# attn0 fast path: serial two-half softmax, T1 T2 T4
# speedup vs baseline: 1.0148x; 1.0148x over previous
; #define LAS __attribute__((address_space(3)))
; #define INF(i) ((const float*)arg_ptr(i))
; __device__ __forceinline__ int v_rd_base(int lane) { return ((lane & 3) << 3) | (((lane >> 2) & 3) << 6) | (((lane >> 4) & 1) << 5) | (((lane >> 5) & 1) << 8); }
; template <int layer>
; __device__ __forceinline__ void attn_phase(LAS unsigned char* lds) {
;     ...
;     const int wid = __builtin_amdgcn_readfirstlane(tid >> 6), r32 = lane & 31, hi = lane >> 5;
;     auto koff_n = [](int tk, int j) { const int ci = j * 256 + tk, row = ci >> 4, pc = ci & 15, lc = pc ^ (row & 7); return (unsigned)(row * KLD + lc * 8) * 2u; };
;     auto koff_r = [](int tk, int j) { const int ci = j * 256 + tk, row = ci >> 3, pc = ci & 7, lc = pc ^ (row & 7); return (unsigned)(row * 64 + lc * 8) * 2u; };
;     auto voff_f = [](int tk, int j) { const int ci = j * 256 + tk, st = ci >> 5, w = ci & 31, kk = (st >> 2) * 8 + (w >> 2), key = (kk & ~0xC) | ((kk & 4) << 1) | ((kk & 8) >> 1), c = (st & 3) * 32 + (w & 3) * 8;
;         return (unsigned)(key * KLD + c) * 2u; };
;     const int tkp = (tid - 256) & 255; const unsigned kof0 = koff_n(tkp, 0), vof0 = voff_f(tkp, 0), rof0 = koff_r(tkp, 0);
;     const int kbn = r32 * 256 + ((hi * 16) ^ ((r32 & 7) << 4)), kbr0 = 16384 + r32 * 128 + ((hi * 16) ^ ((r32 & 7) << 4));
;     const unsigned ldsb = (unsigned)(uintptr_t)lds;
;     const int vb0 = (int)(unsigned)(uintptr_t)(lds + OFF_V) + v_rd_base(lane);
;     LAS float* wsl = (LAS float*)(lds + OFF_WS) + wid * 64; LAS float* li_l = wsl; LAS float* al_l = wsl + 32;
;     const float* cv_wgu = INF(layer == 0 ? 15 : 27); const float* cv_wdn = INF(layer == 0 ? 16 : 28); bf16* cv_gut = WSP(bf16, CV_MODE >= 2 ? WS_Q : WS_W_GUT); bf16* cv_dt = WSP(bf16, CV_MODE >= 2 ? WS_Q : WS_W_DT);
;     constexpr int CV_IG = 32 * 32, CV_ID = 8 * 64, CV_NIT = NEXP * (CV_IG + CV_ID);
;     int cv_it = (CV_MODE == 1) ? CV_NIT : bx * 4 + wid, cv_pend = -1; const int cv_stride = G * 4;
;     const unsigned cv_lds = (unsigned)(uintptr_t)(lds + OFF_CV) + (unsigned)(wid & 3) * 16384u;
.LBB0_525:
	s_or_b64 exec, exec, s[4:5]
	s_mov_b32 s0, 30
	s_waitcnt lgkmcnt(0)
	s_barrier
	s_ashr_i32 s1, s0, 31
	s_lshl_b64 s[0:1], s[0:1], 3
	s_add_u32 s0, s80, s0
	s_addc_u32 s1, s81, s1
	v_mov_b32_e32 v4, v0
	s_load_dwordx2 s[4:5], s[0:1], 0x0
	s_mov_b32 s9, s78
	v_readfirstlane_b32 s0, v4
	s_mov_b32 s28, s79
	s_mov_b32 s8, 8
	s_mov_b32 s6, 1
	s_ashr_i32 s14, s0, 6
	s_mov_b32 s0, 15
	s_ashr_i32 s1, s0, 31
	s_lshl_b64 s[0:1], s[0:1], 3
	s_add_u32 s0, s80, s0
	s_addc_u32 s1, s81, s1
	s_load_dwordx2 s[10:11], s[0:1], 0x0
	s_mov_b32 s0, 16
	s_ashr_i32 s1, s0, 31
	s_lshl_b64 s[0:1], s[0:1], 3
	s_add_u32 s0, s80, s0
	s_addc_u32 s1, s81, s1
	s_load_dwordx2 s[12:13], s[0:1], 0x0
	s_waitcnt lgkmcnt(0)
	s_add_u32 s0, s4, 0x3e00000
	s_addc_u32 s1, s5, 0
	s_add_u32 s2, s4, 0x13e00000
	s_addc_u32 s3, s5, 0
	s_lshl_b32 s7, s28, 2
	s_add_i32 s15, s14, s7
	s_lshl_b32 s7, s14, 14
	s_and_b32 s7, s7, 0xc000
	v_writelane_b32 v252, s9, 9
	s_add_i32 s24, s7, 0
	s_lshl_b32 s22, s9, 2
	s_add_i32 s23, s24, 0x15000
	v_writelane_b32 v252, s79, 10
	s_mov_b32 s29, 0
	s_cmpk_gt_i32 s28, 0x1ff
	s_mov_b32 s33, -1
	v_writelane_b32 v252, s80, 11
	s_nop 1
	v_writelane_b32 v252, s81, 12
	s_cbranch_scc1 .LBB0_583
	s_add_u32 s7, s4, 0x64300000
	v_bfe_u32 v1, v4, 4, 4
	v_and_b32_e32 v3, 15, v4
	v_writelane_b32 v252, s7, 13
	s_addc_u32 s7, s5, 0
	v_bitop3_b32 v3, v1, v3, 15 bitop3:0x6c
	v_lshlrev_b32_e32 v1, 13, v1
	v_writelane_b32 v252, s7, 14
	s_add_u32 s7, s4, 0x31e00000
	v_lshl_or_b32 v1, v3, 4, v1
	v_lshrrev_b32_e32 v3, 5, v4
	v_lshrrev_b32_e32 v7, 1, v4
	v_writelane_b32 v252, s7, 15
	s_addc_u32 s7, s5, 0
	v_and_b32_e32 v3, 4, v3
	v_bfe_u32 v6, v4, 2, 2
	v_and_b32_e32 v7, 8, v7
	v_writelane_b32 v252, s7, 16
	s_add_u32 s7, s4, 0x42000000
	v_or3_b32 v3, v6, v7, v3
	v_and_b32_e32 v6, 0x60, v4
	v_lshlrev_b32_e32 v7, 3, v4
	v_writelane_b32 v252, s7, 17
	s_addc_u32 s7, s5, 0
	s_ashr_i32 s9, s8, 31
	v_and_or_b32 v6, v7, 24, v6
	s_lshl_b64 s[8:9], s[8:9], 3
	v_lshlrev_b32_e32 v6, 1, v6
	s_add_u32 s8, s80, s8
	v_lshl_or_b32 v181, v3, 13, v6
	v_bfe_u32 v3, v4, 3, 5
	v_writelane_b32 v252, s7, 18
	s_addc_u32 s9, s81, s9
	s_ashr_i32 s7, s6, 31
	v_lshrrev_b32_e32 v6, 1, v3
	v_xor_b32_e32 v6, v6, v4
	s_lshl_b64 s[6:7], s[6:7], 3
	v_bfe_u32 v5, v4, 5, 1
	v_lshlrev_b32_e32 v3, 7, v3
	v_lshlrev_b32_e32 v6, 4, v6
	s_movk_i32 s62, 0x70
	s_add_u32 s6, s80, s6
	v_and_b32_e32 v180, 31, v4
	v_and_or_b32 v188, v6, s62, v3
	v_bitop3_b32 v3, v5, v4, 15 bitop3:0x78
	s_addc_u32 s7, s81, s7
	s_load_dwordx2 s[16:17], s[8:9], 0x0
	s_load_dwordx2 s[18:19], s[6:7], 0x0
	v_lshlrev_b32_e32 v3, 4, v3
	v_lshlrev_b32_e32 v6, 7, v180
	s_movk_i32 s6, 0x4000
	v_and_b32_e32 v2, 63, v4
	v_lshl_or_b32 v189, v180, 8, v3
	v_or3_b32 v190, v3, v6, s6
	v_bfe_u32 v226, v4, 1, 3
	v_xor_b32_e32 v226, v226, v5
	v_lshlrev_b32_e32 v226, 4, v226
	v_or3_b32 v190, v226, v6, s6
	v_or_b32_e32 v189, 0x8000, v189
	v_or_b32_e32 v190, 0x8000, v190
	v_xor_b32_e32 v226, 32, v189
	v_xor_b32_e32 v227, 64, v189
	v_xor_b32_e32 v228, 0x60, v189
	v_xor_b32_e32 v232, 0x80, v189
	v_xor_b32_e32 v233, 0xa0, v189
	v_xor_b32_e32 v234, 0xc0, v189
	v_xor_b32_e32 v235, 0xe0, v189
	v_xor_b32_e32 v229, 32, v190
	v_xor_b32_e32 v230, 64, v190
	v_xor_b32_e32 v231, 0x60, v190
	v_lshlrev_b32_e32 v3, 4, v4
	v_lshlrev_b32_e32 v2, 3, v2
	v_and_b32_e32 v3, 0xc0, v3
	v_lshlrev_b32_e32 v6, 1, v4
	v_and_or_b32 v3, v2, 24, v3
	v_and_b32_e32 v6, 32, v6
	v_and_b32_e32 v2, 0x100, v2
	v_or3_b32 v2, v3, v6, v2
	v_add_u32_e32 v191, 0, v2
	v_mov_b32_e32 v3, 0
	v_lshlrev_b32_e32 v2, 4, v5
	v_lshlrev_b32_e32 v8, 3, v5
	v_lshl_add_u64 v[6:7], s[4:5], 0, v[2:3]
	s_mov_b64 s[4:5], 0x5e300000
	v_lshl_add_u64 v[182:183], v[6:7], 0, s[4:5]
	v_and_b32_e32 v2, 32, v4
	v_cvt_f32_ubyte0_e32 v4, v8
	v_or_b32_e32 v7, 1, v8
	s_waitcnt lgkmcnt(0)
; #define LAS __attribute__((address_space(3)))
; #define INF(i) ((const float*)arg_ptr(i))
; __device__ __forceinline__ int v_rd_base(int lane) { return ((lane & 3) << 3) | (((lane >> 2) & 3) << 6) | (((lane >> 4) & 1) << 5) | (((lane >> 5) & 1) << 8); }
; template <int layer>
; __device__ __forceinline__ void attn_phase(LAS unsigned char* lds) {
;     ...
;     const int tkp = (tid - 256) & 255; const unsigned kof0 = koff_n(tkp, 0), vof0 = voff_f(tkp, 0), rof0 = koff_r(tkp, 0);
;     const int kbn = r32 * 256 + ((hi * 16) ^ ((r32 & 7) << 4)), kbr0 = 16384 + r32 * 128 + ((hi * 16) ^ ((r32 & 7) << 4));
;     const unsigned ldsb = (unsigned)(uintptr_t)lds;
;     const int vb0 = (int)(unsigned)(uintptr_t)(lds + OFF_V) + v_rd_base(lane);
;     LAS float* wsl = (LAS float*)(lds + OFF_WS) + wid * 64; LAS float* li_l = wsl; LAS float* al_l = wsl + 32;
;     const float* cv_wgu = INF(layer == 0 ? 15 : 27); const float* cv_wdn = INF(layer == 0 ? 16 : 28); bf16* cv_gut = WSP(bf16, CV_MODE >= 2 ? WS_Q : WS_W_GUT); bf16* cv_dt = WSP(bf16, CV_MODE >= 2 ? WS_Q : WS_W_DT);
;     constexpr int CV_IG = 32 * 32, CV_ID = 8 * 64, CV_NIT = NEXP * (CV_IG + CV_ID);
;     int cv_it = (CV_MODE == 1) ? CV_NIT : bx * 4 + wid, cv_pend = -1; const int cv_stride = G * 4;
;     const unsigned cv_lds = (unsigned)(uintptr_t)(lds + OFF_CV) + (unsigned)(wid & 3) * 16384u;
;     ...
;                             for (int e = 0; e < 2; ++e) { const int j = 2 * jj + e; const int i = c * 16 + hi * 8 + j;
;                                 const float freq = exp2f(-(float)i * (13.287712379549449f / 32.0f)); float rev = pos * freq * 0.15915494309189535f; rev -= floorf(rev);
	v_lshl_add_u64 v[184:185], s[16:17], 0, v[2:3]
	v_mul_i32_i24_e32 v2, -4, v5
	v_mul_f32_e32 v5, 0xbed49a78, v4
	s_mov_b32 s6, 0xc2fc0000
	v_cvt_f32_ubyte0_e32 v7, v7
	v_mov_b32_e32 v6, 0x42800000
	v_cmp_gt_f32_e32 vcc, s6, v5
	v_mul_f32_e32 v9, 0xbed49a78, v7
	v_cmp_gt_f32_e64 s[4:5], s6, v9
	v_cndmask_b32_e32 v5, 0, v6, vcc
	v_fmac_f32_e32 v5, 0xbed49a78, v4
	v_cndmask_b32_e64 v9, 0, v6, s[4:5]
	v_exp_f32_e32 v4, v5
	v_fmac_f32_e32 v9, 0xbed49a78, v7
	v_exp_f32_e32 v7, v9
	v_not_b32_e32 v5, 63
	v_cndmask_b32_e32 v9, 0, v5, vcc
	v_ldexp_f32 v192, v4, v9
	v_cndmask_b32_e64 v4, 0, v5, s[4:5]
	v_ldexp_f32 v193, v7, v4
	v_or_b32_e32 v4, 2, v8
	v_cvt_f32_ubyte0_e32 v4, v4
	v_mul_f32_e32 v7, 0xbed49a78, v4
	v_cmp_gt_f32_e32 vcc, s6, v7
	s_lshl_b32 s7, s14, 5
	v_writelane_b32 v252, s18, 19
	v_cndmask_b32_e32 v7, 0, v6, vcc
	v_fmac_f32_e32 v7, 0xbed49a78, v4
	v_exp_f32_e32 v4, v7
	v_or_b32_e32 v7, 3, v8
	v_cvt_f32_ubyte0_e32 v7, v7
	v_mul_f32_e32 v9, 0xbed49a78, v7
	v_cmp_gt_f32_e64 s[4:5], s6, v9
	s_cmp_gt_i32 s14, 3
	v_writelane_b32 v252, s19, 20
	v_cndmask_b32_e64 v9, 0, v6, s[4:5]
	v_fmac_f32_e32 v9, 0xbed49a78, v7
	v_exp_f32_e32 v7, v9
	v_cndmask_b32_e32 v9, 0, v5, vcc
	v_ldexp_f32 v194, v4, v9
	v_cndmask_b32_e64 v4, 0, v5, s[4:5]
	v_ldexp_f32 v195, v7, v4
	v_or_b32_e32 v4, 4, v8
	v_cvt_f32_ubyte0_e32 v4, v4
	v_mul_f32_e32 v7, 0xbed49a78, v4
	v_cmp_gt_f32_e32 vcc, s6, v7
	s_cselect_b64 s[18:19], -1, 0
	s_lshl_b32 s64, s14, 10
	v_cndmask_b32_e32 v7, 0, v6, vcc
	v_fmac_f32_e32 v7, 0xbed49a78, v4
	v_exp_f32_e32 v4, v7
	v_or_b32_e32 v7, 5, v8
	v_cvt_f32_ubyte0_e32 v7, v7
	v_mul_f32_e32 v9, 0xbed49a78, v7
	v_cmp_gt_f32_e64 s[4:5], s6, v9
	s_add_i32 s64, s64, 0
	s_add_i32 s65, s64, 0x7000
	v_cndmask_b32_e64 v9, 0, v6, s[4:5]
	v_fmac_f32_e32 v9, 0xbed49a78, v7
	v_exp_f32_e32 v7, v9
	v_cndmask_b32_e32 v9, 0, v5, vcc
	v_ldexp_f32 v196, v4, v9
	v_cndmask_b32_e64 v4, 0, v5, s[4:5]
	v_ldexp_f32 v197, v7, v4
	v_or_b32_e32 v4, 6, v8
	v_cvt_f32_ubyte0_e32 v4, v4
	v_mul_f32_e32 v7, 0xbed49a78, v4
	v_cmp_gt_f32_e32 vcc, s6, v7
	s_add_i32 s66, s64, 0xb000
	s_add_i32 s67, s64, 0xfffff000
	v_cndmask_b32_e32 v7, 0, v6, vcc
	v_fmac_f32_e32 v7, 0xbed49a78, v4
	v_exp_f32_e32 v4, v7
	v_or_b32_e32 v7, 7, v8
	v_cvt_f32_ubyte0_e32 v7, v7
	v_mul_f32_e32 v9, 0xbed49a78, v7
	v_cmp_gt_f32_e64 s[4:5], s6, v9
	s_add_i32 s68, s64, 0xd000
	s_add_i32 s69, s64, 0x11000
	v_cndmask_b32_e64 v9, 0, v6, s[4:5]
	v_fmac_f32_e32 v9, 0xbed49a78, v7
	v_exp_f32_e32 v7, v9
	v_cndmask_b32_e32 v9, 0, v5, vcc
	v_ldexp_f32 v198, v4, v9
	v_cndmask_b32_e64 v4, 0, v5, s[4:5]
	v_ldexp_f32 v199, v7, v4
	v_or_b32_e32 v4, 16, v8
	v_cvt_f32_ubyte0_e32 v4, v4
	v_mul_f32_e32 v7, 0xbed49a78, v4
	v_cmp_gt_f32_e32 vcc, s6, v7
	s_add_i32 s70, s64, 0x3000
	v_writelane_b32 v252, s14, 21
	v_cndmask_b32_e32 v7, 0, v6, vcc
	v_fmac_f32_e32 v7, 0xbed49a78, v4
	v_exp_f32_e32 v4, v7
	v_or_b32_e32 v7, 17, v8
	v_cvt_f32_ubyte0_e32 v7, v7
	v_mul_f32_e32 v9, 0xbed49a78, v7
	v_cmp_gt_f32_e64 s[4:5], s6, v9
	s_cmp_lt_i32 s14, 4
	s_movk_i32 s61, 0x60
	v_cndmask_b32_e64 v9, 0, v6, s[4:5]
	v_fmac_f32_e32 v9, 0xbed49a78, v7
	v_exp_f32_e32 v7, v9
	v_cndmask_b32_e32 v9, 0, v5, vcc
	v_ldexp_f32 v200, v4, v9
	v_cndmask_b32_e64 v4, 0, v5, s[4:5]
	v_ldexp_f32 v201, v7, v4
	v_or_b32_e32 v4, 18, v8
	v_cvt_f32_ubyte0_e32 v4, v4
	v_mul_f32_e32 v7, 0xbed49a78, v4
	v_cmp_gt_f32_e32 vcc, s6, v7
	s_cselect_b64 s[20:21], -1, 0
	s_add_i32 s71, s24, 0x17000
	v_cndmask_b32_e32 v7, 0, v6, vcc
	v_fmac_f32_e32 v7, 0xbed49a78, v4
	v_exp_f32_e32 v4, v7
	v_or_b32_e32 v7, 19, v8
	v_cvt_f32_ubyte0_e32 v7, v7
	v_mul_f32_e32 v9, 0xbed49a78, v7
	v_cmp_gt_f32_e64 s[4:5], s6, v9
	s_mov_b32 s72, 0x42800000
	v_or_b32_e32 v208, 0x20000, v1
	v_cndmask_b32_e64 v9, 0, v6, s[4:5]
	v_fmac_f32_e32 v9, 0xbed49a78, v7
	v_exp_f32_e32 v7, v9
	v_cndmask_b32_e32 v9, 0, v5, vcc
	v_ldexp_f32 v202, v4, v9
	v_cndmask_b32_e64 v4, 0, v5, s[4:5]
	v_ldexp_f32 v203, v7, v4
	v_or_b32_e32 v4, 20, v8
	v_cvt_f32_ubyte0_e32 v4, v4
	v_mul_f32_e32 v7, 0xbed49a78, v4
	v_cmp_gt_f32_e32 vcc, s6, v7
	s_add_i32 s73, s64, 0x8000
	v_or_b32_e32 v209, 0x40000, v1
	v_cndmask_b32_e32 v7, 0, v6, vcc
	v_fmac_f32_e32 v7, 0xbed49a78, v4
	v_exp_f32_e32 v4, v7
	v_or_b32_e32 v7, 21, v8
	v_cvt_f32_ubyte0_e32 v7, v7
	v_mul_f32_e32 v9, 0xbed49a78, v7
	v_cmp_gt_f32_e64 s[4:5], s6, v9
	s_add_i32 s74, s64, 0x9000
	v_or_b32_e32 v210, 0x60000, v1
	v_cndmask_b32_e64 v9, 0, v6, s[4:5]
	v_fmac_f32_e32 v9, 0xbed49a78, v7
	v_exp_f32_e32 v7, v9
	v_cndmask_b32_e32 v9, 0, v5, vcc
	v_ldexp_f32 v204, v4, v9
	v_cndmask_b32_e64 v4, 0, v5, s[4:5]
	v_ldexp_f32 v205, v7, v4
	v_or_b32_e32 v4, 22, v8
	v_cvt_f32_ubyte0_e32 v4, v4
	v_mul_f32_e32 v7, 0xbed49a78, v4
	v_cmp_gt_f32_e32 vcc, s6, v7
	s_add_i32 s75, s64, 0xa000
	v_or_b32_e32 v211, 0x1000, v188
	v_cndmask_b32_e32 v7, 0, v6, vcc
	v_fmac_f32_e32 v7, 0xbed49a78, v4
	v_exp_f32_e32 v4, v7
	v_or_b32_e32 v7, 23, v8
	v_cvt_f32_ubyte0_e32 v7, v7
	v_mul_f32_e32 v8, 0xbed49a78, v7
	v_cmp_gt_f32_e64 s[4:5], s6, v8
	s_add_i32 s76, s64, 0xc000
	v_or_b32_e32 v212, 0x20000, v181
	v_cndmask_b32_e64 v6, 0, v6, s[4:5]
	v_fmac_f32_e32 v6, 0xbed49a78, v7
	v_exp_f32_e32 v6, v6
	v_cndmask_b32_e32 v7, 0, v5, vcc
	v_ldexp_f32 v206, v4, v7
	v_cndmask_b32_e64 v4, 0, v5, s[4:5]
	v_ldexp_f32 v207, v6, v4
	v_or_b32_e32 v213, 0x40000, v181
	s_add_i32 s77, s64, 0x1000
	v_or_b32_e32 v214, 0x60000, v181
	s_add_i32 s78, s64, 0x2000
	s_add_i32 s79, s64, 0xe000
	s_add_i32 s80, s64, 0xf000
	s_add_i32 s81, s64, 0x10000
	s_add_i32 s82, s64, 0x12000
	s_add_i32 s83, s64, 0x4000
	s_add_i32 s84, s64, 0x5000
	s_add_i32 s85, s64, 0x6000
	s_add_i32 s86, s24, 0x15400
	s_add_i32 s87, s24, 0x15800
	s_add_i32 s88, s24, 0x15c00
	s_add_i32 s89, s24, 0x16000
	s_add_i32 s90, s24, 0x16400
	s_add_i32 s91, s24, 0x16800
	s_add_i32 s92, s24, 0x16c00
	s_add_i32 s93, s24, 0x17400
	s_add_i32 s94, s24, 0x17800
	s_add_i32 s95, s24, 0x17c00
	s_add_i32 s96, s24, 0x18000
	s_add_i32 s97, s24, 0x18400
	s_add_i32 s27, s24, 0x18800
	v_writelane_b32 v252, s24, 22
	s_add_i32 s26, s24, 0x18c00
	v_add3_u32 v215, v2, s7, v180
	v_mov_b32_e32 v216, 0x358637bd
	s_movk_i32 s30, 0x3ff
	s_movk_i32 s31, 0x50
	v_mov_b32_e32 v217, 0x1800
	v_mov_b32_e32 v218, 0x10000
	v_mov_b32_e32 v219, 0xff800000
	v_writelane_b32 v252, s7, 23

.LBB0_556:
	s_cmp_le_i32 s63, s28
	s_cbranch_scc0 .Lorig_a0b0
	s_cmp_eq_u32 s17, 0
	s_cbranch_scc1 .Lorig_a0b0
	ds_read_b128 v[116:119], v189 offset:0
	ds_read_b128 v[120:123], v226 offset:0
	ds_read_b128 v[124:127], v227 offset:0
	ds_read_b128 v[128:131], v228 offset:0
	s_waitcnt lgkmcnt(3)
	v_mfma_f32_32x32x16_bf16 v[84:99], v[116:119], v[132:135], 0
	ds_read_b128 v[116:119], v232 offset:0
	s_waitcnt lgkmcnt(3)
	v_mfma_f32_32x32x16_bf16 v[84:99], v[120:123], v[136:139], v[84:99]
	ds_read_b128 v[120:123], v233 offset:0
	s_waitcnt lgkmcnt(3)
	v_mfma_f32_32x32x16_bf16 v[84:99], v[124:127], v[140:143], v[84:99]
	ds_read_b128 v[124:127], v234 offset:0
	s_waitcnt lgkmcnt(3)
	v_mfma_f32_32x32x16_bf16 v[84:99], v[128:131], v[144:147], v[84:99]
	ds_read_b128 v[128:131], v235 offset:0
	s_waitcnt lgkmcnt(3)
	v_mfma_f32_32x32x16_bf16 v[84:99], v[116:119], v[148:151], v[84:99]
	ds_read_b128 v[116:119], v190 offset:0
	s_waitcnt lgkmcnt(3)
	v_mfma_f32_32x32x16_bf16 v[84:99], v[120:123], v[152:155], v[84:99]
	ds_read_b128 v[120:123], v229 offset:0
	s_waitcnt lgkmcnt(3)
	v_mfma_f32_32x32x16_bf16 v[84:99], v[124:127], v[156:159], v[84:99]
	ds_read_b128 v[124:127], v230 offset:0
	s_waitcnt lgkmcnt(3)
	v_mfma_f32_32x32x16_bf16 v[84:99], v[128:131], v[160:163], v[84:99]
	ds_read_b128 v[128:131], v231 offset:0
	s_waitcnt lgkmcnt(3)
	v_mfma_f32_32x32x16_bf16 v[84:99], v[116:119], v[164:167], v[84:99]
	ds_read_b128 v[116:119], v189 offset:8192
	s_waitcnt lgkmcnt(3)
	v_mfma_f32_32x32x16_bf16 v[84:99], v[120:123], v[172:175], v[84:99]
	ds_read_b128 v[120:123], v226 offset:8192
	s_waitcnt lgkmcnt(3)
	v_mfma_f32_32x32x16_bf16 v[84:99], v[124:127], v[168:171], v[84:99]
	ds_read_b128 v[124:127], v227 offset:8192
	s_waitcnt lgkmcnt(3)
	v_mfma_f32_32x32x16_bf16 v[84:99], v[128:131], v[176:179], v[84:99]
	ds_read_b128 v[128:131], v228 offset:8192
	s_waitcnt lgkmcnt(3)
	v_mfma_f32_32x32x16_bf16 v[68:83], v[116:119], v[132:135], 0
	ds_read_b128 v[116:119], v232 offset:8192
	s_waitcnt lgkmcnt(3)
	v_mfma_f32_32x32x16_bf16 v[68:83], v[120:123], v[136:139], v[68:83]
	ds_read_b128 v[120:123], v233 offset:8192
	s_waitcnt lgkmcnt(3)
	v_mfma_f32_32x32x16_bf16 v[68:83], v[124:127], v[140:143], v[68:83]
	ds_read_b128 v[124:127], v234 offset:8192
	s_waitcnt lgkmcnt(3)
	v_mfma_f32_32x32x16_bf16 v[68:83], v[128:131], v[144:147], v[68:83]
	ds_read_b128 v[128:131], v235 offset:8192
	s_waitcnt lgkmcnt(3)
	v_mfma_f32_32x32x16_bf16 v[68:83], v[116:119], v[148:151], v[68:83]
	ds_read_b128 v[116:119], v190 offset:4096
	s_waitcnt lgkmcnt(3)
	v_mfma_f32_32x32x16_bf16 v[68:83], v[120:123], v[152:155], v[68:83]
	ds_read_b128 v[120:123], v229 offset:4096
	s_waitcnt lgkmcnt(3)
	v_mfma_f32_32x32x16_bf16 v[68:83], v[124:127], v[156:159], v[68:83]
	ds_read_b128 v[124:127], v230 offset:4096
	s_waitcnt lgkmcnt(3)
	v_mfma_f32_32x32x16_bf16 v[68:83], v[128:131], v[160:163], v[68:83]
	ds_read_b128 v[128:131], v231 offset:4096
	s_waitcnt lgkmcnt(3)
	v_mfma_f32_32x32x16_bf16 v[68:83], v[116:119], v[164:167], v[68:83]
	s_waitcnt lgkmcnt(2)
	v_mfma_f32_32x32x16_bf16 v[68:83], v[120:123], v[172:175], v[68:83]
	s_waitcnt lgkmcnt(1)
	v_mfma_f32_32x32x16_bf16 v[68:83], v[124:127], v[168:171], v[68:83]
	s_waitcnt lgkmcnt(0)
	v_mfma_f32_32x32x16_bf16 v[68:83], v[128:131], v[176:179], v[68:83]
	ds_read_b64_tr_b16 v[116:117], v191 offset:0
	ds_read_b64_tr_b16 v[118:119], v191 offset:2048
	ds_read_b64_tr_b16 v[120:121], v191 offset:4096
	ds_read_b64_tr_b16 v[122:123], v191 offset:6144
	ds_read_b64_tr_b16 v[124:125], v191 offset:512
	ds_read_b64_tr_b16 v[126:127], v191 offset:2560
	ds_read_b64_tr_b16 v[128:129], v191 offset:4608
	ds_read_b64_tr_b16 v[130:131], v191 offset:6656
	s_nop 7
	s_nop 3
	v_max3_f32 v2, v84, v85, v86
	v_max3_f32 v251, v68, v69, v70
	v_max3_f32 v2, v2, v87, v88
	v_max3_f32 v251, v251, v71, v72
	v_max3_f32 v2, v2, v89, v90
	v_max3_f32 v251, v251, v73, v74
	v_max3_f32 v2, v2, v91, v92
	v_max3_f32 v251, v251, v75, v76
	v_max3_f32 v2, v2, v93, v94
	v_max3_f32 v251, v251, v77, v78
	v_max3_f32 v2, v2, v95, v96
	v_max3_f32 v251, v251, v79, v80
	v_max3_f32 v2, v2, v97, v98
	v_max3_f32 v251, v251, v81, v82
	v_max3_f32 v2, v2, v99, v83
	v_max_f32_e32 v2, v2, v251
	v_mov_b32_e32 v251, v2
	s_nop 1
	v_permlane32_swap_b32_e32 v2, v251
	v_max_f32_e32 v251, v251, v251
	v_max_f32_e32 v2, v2, v2
	v_max_f32_e32 v2, v2, v251
	v_sub_f32_e32 v2, v2, v223
	v_cmp_ge_f32_e32 vcc, s72, v2
	s_cmp_eq_u64 vcc, exec
	s_cbranch_scc0 .Lfb_a0b0
	v_sub_f32_e32 v100, v84, v223
	v_sub_f32_e32 v101, v85, v223
	v_sub_f32_e32 v102, v86, v223
	v_sub_f32_e32 v103, v87, v223
	v_sub_f32_e32 v104, v88, v223
	v_sub_f32_e32 v105, v89, v223
	v_sub_f32_e32 v106, v90, v223
	v_sub_f32_e32 v107, v91, v223
	v_sub_f32_e32 v108, v92, v223
	v_sub_f32_e32 v109, v93, v223
	v_sub_f32_e32 v110, v94, v223
	v_sub_f32_e32 v111, v95, v223
	v_sub_f32_e32 v112, v96, v223
	v_sub_f32_e32 v113, v97, v223
	v_sub_f32_e32 v114, v98, v223
	v_sub_f32_e32 v115, v99, v223
	v_exp_f32_e32 v100, v100
	v_exp_f32_e32 v101, v101
	v_exp_f32_e32 v102, v102
	v_exp_f32_e32 v103, v103
	v_exp_f32_e32 v104, v104
	v_exp_f32_e32 v105, v105
	v_exp_f32_e32 v106, v106
	v_exp_f32_e32 v107, v107
	v_exp_f32_e32 v108, v108
	v_exp_f32_e32 v109, v109
	v_exp_f32_e32 v110, v110
	v_exp_f32_e32 v111, v111
	v_exp_f32_e32 v112, v112
	v_exp_f32_e32 v113, v113
	v_exp_f32_e32 v114, v114
	v_exp_f32_e32 v115, v115
	v_add_f32_e32 v237, v100, v101
	v_add_f32_e32 v251, v102, v103
	v_add_f32_e32 v237, v237, v104
	v_add_f32_e32 v251, v251, v105
	v_add_f32_e32 v237, v237, v106
	v_add_f32_e32 v251, v251, v107
	v_add_f32_e32 v237, v237, v108
	v_add_f32_e32 v251, v251, v109
	v_add_f32_e32 v237, v237, v110
	v_add_f32_e32 v251, v251, v111
	v_add_f32_e32 v237, v237, v112
	v_add_f32_e32 v251, v251, v113
	v_add_f32_e32 v237, v237, v114
	v_add_f32_e32 v251, v251, v115
	v_add_f32_e32 v237, v237, v251
	v_cvt_pk_bf16_f32 v238, v100, v101
	v_cvt_pk_bf16_f32 v239, v102, v103
	v_cvt_pk_bf16_f32 v240, v104, v105
	v_cvt_pk_bf16_f32 v241, v106, v107
	v_cvt_pk_bf16_f32 v242, v108, v109
	v_cvt_pk_bf16_f32 v243, v110, v111
	v_cvt_pk_bf16_f32 v244, v112, v113
	v_cvt_pk_bf16_f32 v245, v114, v115
	s_nop 1
	v_permlane32_swap_b32_e32 v238, v240
	v_permlane32_swap_b32_e32 v239, v241
	v_permlane32_swap_b32_e32 v242, v244
	v_permlane32_swap_b32_e32 v243, v245
	v_sub_f32_e32 v100, v68, v223
	v_sub_f32_e32 v101, v69, v223
	v_sub_f32_e32 v102, v70, v223
	v_sub_f32_e32 v103, v71, v223
	v_sub_f32_e32 v104, v72, v223
	v_sub_f32_e32 v105, v73, v223
	v_sub_f32_e32 v106, v74, v223
	v_sub_f32_e32 v107, v75, v223
	v_sub_f32_e32 v108, v76, v223
	v_sub_f32_e32 v109, v77, v223
	v_sub_f32_e32 v110, v78, v223
	v_sub_f32_e32 v111, v79, v223
	v_sub_f32_e32 v112, v80, v223
	v_sub_f32_e32 v113, v81, v223
	v_sub_f32_e32 v114, v82, v223
	v_sub_f32_e32 v115, v83, v223
	v_exp_f32_e32 v100, v100
	v_exp_f32_e32 v101, v101
	v_exp_f32_e32 v102, v102
	v_exp_f32_e32 v103, v103
	v_exp_f32_e32 v104, v104
	v_exp_f32_e32 v105, v105
	v_exp_f32_e32 v106, v106
	v_exp_f32_e32 v107, v107
	v_exp_f32_e32 v108, v108
	v_exp_f32_e32 v109, v109
	v_exp_f32_e32 v110, v110
	v_exp_f32_e32 v111, v111
	v_exp_f32_e32 v112, v112
	v_exp_f32_e32 v113, v113
	v_exp_f32_e32 v114, v114
	v_exp_f32_e32 v115, v115
	v_add_f32_e32 v250, v100, v101
	v_add_f32_e32 v251, v102, v103
	v_add_f32_e32 v250, v250, v104
	v_add_f32_e32 v251, v251, v105
	v_add_f32_e32 v250, v250, v106
	v_add_f32_e32 v251, v251, v107
	v_add_f32_e32 v250, v250, v108
	v_add_f32_e32 v251, v251, v109
	v_add_f32_e32 v250, v250, v110
	v_add_f32_e32 v251, v251, v111
	v_add_f32_e32 v250, v250, v112
	v_add_f32_e32 v251, v251, v113
	v_add_f32_e32 v250, v250, v114
	v_add_f32_e32 v251, v251, v115
	v_add_f32_e32 v250, v250, v251
	v_cvt_pk_bf16_f32 v84, v100, v101
	v_cvt_pk_bf16_f32 v85, v102, v103
	v_cvt_pk_bf16_f32 v86, v104, v105
	v_cvt_pk_bf16_f32 v87, v106, v107
	v_cvt_pk_bf16_f32 v88, v108, v109
	v_cvt_pk_bf16_f32 v89, v110, v111
	v_cvt_pk_bf16_f32 v90, v112, v113
	v_cvt_pk_bf16_f32 v91, v114, v115
	s_nop 1
	v_permlane32_swap_b32_e32 v84, v86
	v_permlane32_swap_b32_e32 v85, v87
	v_permlane32_swap_b32_e32 v88, v90
	v_permlane32_swap_b32_e32 v89, v91
	v_add_f32_e32 v237, v237, v250
	v_mov_b32_e32 v250, v237
	s_nop 1
	v_permlane32_swap_b32_e32 v237, v250
	v_add_f32_e32 v237, v237, v250
	v_add_f32_e32 v100, v237, v221
	v_mov_b32_e32 v222, v223
	s_waitcnt lgkmcnt(6)
	v_mfma_f32_32x32x16_bf16 v[52:67], v[116:119], v[238:241], v[52:67]
	ds_read_b64_tr_b16 v[116:117], v191 offset:1024
	ds_read_b64_tr_b16 v[118:119], v191 offset:3072
	s_waitcnt lgkmcnt(6)
	v_mfma_f32_32x32x16_bf16 v[52:67], v[120:123], v[242:245], v[52:67]
	ds_read_b64_tr_b16 v[120:121], v191 offset:5120
	ds_read_b64_tr_b16 v[122:123], v191 offset:7168
	s_waitcnt lgkmcnt(6)
	v_mfma_f32_32x32x16_bf16 v[36:51], v[124:127], v[238:241], v[36:51]
	ds_read_b64_tr_b16 v[124:125], v191 offset:1536
	ds_read_b64_tr_b16 v[126:127], v191 offset:3584
	s_waitcnt lgkmcnt(6)
	v_mfma_f32_32x32x16_bf16 v[36:51], v[128:131], v[242:245], v[36:51]
	ds_read_b64_tr_b16 v[128:129], v191 offset:5632
	ds_read_b64_tr_b16 v[130:131], v191 offset:7680
	s_waitcnt lgkmcnt(6)
	v_mfma_f32_32x32x16_bf16 v[20:35], v[116:119], v[238:241], v[20:35]
	ds_read_b64_tr_b16 v[116:117], v191 offset:8192
	ds_read_b64_tr_b16 v[118:119], v191 offset:10240
	s_waitcnt lgkmcnt(6)
	v_mfma_f32_32x32x16_bf16 v[20:35], v[120:123], v[242:245], v[20:35]
	ds_read_b64_tr_b16 v[120:121], v191 offset:12288
	ds_read_b64_tr_b16 v[122:123], v191 offset:14336
	s_waitcnt lgkmcnt(6)
	v_mfma_f32_32x32x16_bf16 v[4:19], v[124:127], v[238:241], v[4:19]
	ds_read_b64_tr_b16 v[124:125], v191 offset:8704
	ds_read_b64_tr_b16 v[126:127], v191 offset:10752
	s_waitcnt lgkmcnt(6)
	v_mfma_f32_32x32x16_bf16 v[4:19], v[128:131], v[242:245], v[4:19]
	ds_read_b64_tr_b16 v[128:129], v191 offset:12800
	ds_read_b64_tr_b16 v[130:131], v191 offset:14848
	s_nop 1
	s_waitcnt lgkmcnt(6)
	v_mfma_f32_32x32x16_bf16 v[52:67], v[116:119], v[84:87], v[52:67]
	ds_read_b64_tr_b16 v[116:117], v191 offset:9216
	ds_read_b64_tr_b16 v[118:119], v191 offset:11264
	s_waitcnt lgkmcnt(6)
	v_mfma_f32_32x32x16_bf16 v[52:67], v[120:123], v[88:91], v[52:67]
	ds_read_b64_tr_b16 v[120:121], v191 offset:13312
	ds_read_b64_tr_b16 v[122:123], v191 offset:15360
	s_waitcnt lgkmcnt(6)
	v_mfma_f32_32x32x16_bf16 v[36:51], v[124:127], v[84:87], v[36:51]
	ds_read_b64_tr_b16 v[124:125], v191 offset:9728
	ds_read_b64_tr_b16 v[126:127], v191 offset:11776
	s_waitcnt lgkmcnt(6)
	v_mfma_f32_32x32x16_bf16 v[36:51], v[128:131], v[88:91], v[36:51]
	ds_read_b64_tr_b16 v[128:129], v191 offset:13824
	ds_read_b64_tr_b16 v[130:131], v191 offset:15872
	s_waitcnt lgkmcnt(6)
	v_mfma_f32_32x32x16_bf16 v[20:35], v[116:119], v[84:87], v[20:35]
	s_waitcnt lgkmcnt(4)
	v_mfma_f32_32x32x16_bf16 v[20:35], v[120:123], v[88:91], v[20:35]
	s_waitcnt lgkmcnt(2)
	v_mfma_f32_32x32x16_bf16 v[4:19], v[124:127], v[84:87], v[4:19]
	s_waitcnt lgkmcnt(0)
	v_mfma_f32_32x32x16_bf16 v[4:19], v[128:131], v[88:91], v[4:19]
	s_branch .Ltail_a0b0
.Lfb_a0b0:
	s_waitcnt lgkmcnt(0)
	s_branch .LBB0_558
.Lorig_a0b0:
	ds_read_b128 v[100:103], v189 offset:0
	ds_read_b128 v[104:107], v189 offset:8192
	ds_read_b128 v[108:111], v226 offset:0
	ds_read_b128 v[112:115], v226 offset:8192
	ds_read_b128 v[116:119], v227 offset:0
	ds_read_b128 v[120:123], v227 offset:8192
	ds_read_b128 v[124:127], v228 offset:0
	ds_read_b128 v[128:131], v228 offset:8192
	s_waitcnt lgkmcnt(7)
	v_mfma_f32_32x32x16_bf16 v[84:99], v[100:103], v[132:135], 0
	ds_read_b128 v[100:103], v232 offset:0
	s_waitcnt lgkmcnt(7)
	v_mfma_f32_32x32x16_bf16 v[68:83], v[104:107], v[132:135], 0
	ds_read_b128 v[104:107], v232 offset:8192
	s_waitcnt lgkmcnt(7)
	v_mfma_f32_32x32x16_bf16 v[84:99], v[108:111], v[136:139], v[84:99]
	ds_read_b128 v[108:111], v233 offset:0
	s_waitcnt lgkmcnt(7)
	v_mfma_f32_32x32x16_bf16 v[68:83], v[112:115], v[136:139], v[68:83]
	ds_read_b128 v[112:115], v233 offset:8192
	s_waitcnt lgkmcnt(7)
	v_mfma_f32_32x32x16_bf16 v[84:99], v[116:119], v[140:143], v[84:99]
	ds_read_b128 v[116:119], v234 offset:0
	s_waitcnt lgkmcnt(7)
	v_mfma_f32_32x32x16_bf16 v[68:83], v[120:123], v[140:143], v[68:83]
	ds_read_b128 v[120:123], v234 offset:8192
	s_waitcnt lgkmcnt(7)
	v_mfma_f32_32x32x16_bf16 v[84:99], v[124:127], v[144:147], v[84:99]
	ds_read_b128 v[124:127], v235 offset:0
	s_waitcnt lgkmcnt(7)
	v_mfma_f32_32x32x16_bf16 v[68:83], v[128:131], v[144:147], v[68:83]
	ds_read_b128 v[128:131], v235 offset:8192
	s_waitcnt lgkmcnt(7)
	v_mfma_f32_32x32x16_bf16 v[84:99], v[100:103], v[148:151], v[84:99]
	ds_read_b128 v[100:103], v190 offset:0
	s_waitcnt lgkmcnt(7)
	v_mfma_f32_32x32x16_bf16 v[68:83], v[104:107], v[148:151], v[68:83]
	ds_read_b128 v[104:107], v190 offset:4096
	s_waitcnt lgkmcnt(7)
	v_mfma_f32_32x32x16_bf16 v[84:99], v[108:111], v[152:155], v[84:99]
	ds_read_b128 v[108:111], v229 offset:0
	s_waitcnt lgkmcnt(7)
	v_mfma_f32_32x32x16_bf16 v[68:83], v[112:115], v[152:155], v[68:83]
	ds_read_b128 v[112:115], v229 offset:4096
	s_waitcnt lgkmcnt(7)
	v_mfma_f32_32x32x16_bf16 v[84:99], v[116:119], v[156:159], v[84:99]
	ds_read_b128 v[116:119], v230 offset:0
	s_waitcnt lgkmcnt(7)
	v_mfma_f32_32x32x16_bf16 v[68:83], v[120:123], v[156:159], v[68:83]
	ds_read_b128 v[120:123], v230 offset:4096
	s_waitcnt lgkmcnt(7)
	v_mfma_f32_32x32x16_bf16 v[84:99], v[124:127], v[160:163], v[84:99]
	ds_read_b128 v[124:127], v231 offset:0
	s_waitcnt lgkmcnt(7)
	v_mfma_f32_32x32x16_bf16 v[68:83], v[128:131], v[160:163], v[68:83]
	ds_read_b128 v[128:131], v231 offset:4096
	s_waitcnt lgkmcnt(7)
	v_mfma_f32_32x32x16_bf16 v[84:99], v[100:103], v[164:167], v[84:99]
	s_waitcnt lgkmcnt(6)
	v_mfma_f32_32x32x16_bf16 v[68:83], v[104:107], v[164:167], v[68:83]
	s_waitcnt lgkmcnt(5)
	v_mfma_f32_32x32x16_bf16 v[84:99], v[108:111], v[172:175], v[84:99]
	s_waitcnt lgkmcnt(4)
	v_mfma_f32_32x32x16_bf16 v[68:83], v[112:115], v[172:175], v[68:83]
	s_waitcnt lgkmcnt(3)
	v_mfma_f32_32x32x16_bf16 v[84:99], v[116:119], v[168:171], v[84:99]
	s_waitcnt lgkmcnt(2)
	v_mfma_f32_32x32x16_bf16 v[68:83], v[120:123], v[168:171], v[68:83]
	s_waitcnt lgkmcnt(1)
	v_mfma_f32_32x32x16_bf16 v[84:99], v[124:127], v[176:179], v[84:99]
	s_waitcnt lgkmcnt(0)
	v_mfma_f32_32x32x16_bf16 v[68:83], v[128:131], v[176:179], v[68:83]
	s_nop 0
	s_cmp_le_i32 s63, s28
	s_cbranch_scc1 .LBB0_558
	v_add_u32_e32 v2, s17, v220
	v_cmp_lt_i32_e32 vcc, -1, v2
	v_add_u32_e32 v100, -1, v2
	s_nop 3
	v_cndmask_b32_e32 v84, v219, v84, vcc
	v_cmp_lt_i32_e32 vcc, 31, v2
	s_nop 1
	v_cndmask_b32_e32 v68, v219, v68, vcc
	v_cmp_lt_i32_e32 vcc, -1, v100
	s_nop 1
	v_cndmask_b32_e32 v85, v219, v85, vcc
	v_cmp_lt_i32_e32 vcc, 31, v100
	v_add_u32_e32 v100, -2, v2
	s_nop 0
	v_cndmask_b32_e32 v69, v219, v69, vcc
	v_cmp_lt_i32_e32 vcc, -1, v100
	s_nop 1
	v_cndmask_b32_e32 v86, v219, v86, vcc
	v_cmp_lt_i32_e32 vcc, 31, v100
	v_add_u32_e32 v100, -3, v2
	s_nop 0
	v_cndmask_b32_e32 v70, v219, v70, vcc
	v_cmp_lt_i32_e32 vcc, -1, v100
	s_nop 1
	v_cndmask_b32_e32 v87, v219, v87, vcc
	v_cmp_lt_i32_e32 vcc, 31, v100
	v_add_u32_e32 v100, -8, v2
	s_nop 0
	v_cndmask_b32_e32 v71, v219, v71, vcc
	v_cmp_lt_i32_e32 vcc, -1, v100
	s_nop 1
	v_cndmask_b32_e32 v88, v219, v88, vcc
	v_cmp_lt_i32_e32 vcc, 31, v100
	v_add_u32_e32 v100, -9, v2
	s_nop 0
	v_cndmask_b32_e32 v72, v219, v72, vcc
	v_cmp_lt_i32_e32 vcc, -1, v100
	s_nop 1
	v_cndmask_b32_e32 v89, v219, v89, vcc
	v_cmp_lt_i32_e32 vcc, 31, v100
	v_add_u32_e32 v100, -10, v2
	s_nop 0
	v_cndmask_b32_e32 v73, v219, v73, vcc
	v_cmp_lt_i32_e32 vcc, -1, v100
	s_nop 1
	v_cndmask_b32_e32 v90, v219, v90, vcc
	v_cmp_lt_i32_e32 vcc, 31, v100
	v_add_u32_e32 v100, -11, v2
	s_nop 0
	v_cndmask_b32_e32 v74, v219, v74, vcc
	v_cmp_lt_i32_e32 vcc, -1, v100
	s_nop 1
	v_cndmask_b32_e32 v91, v219, v91, vcc
	v_cmp_lt_i32_e32 vcc, 31, v100
	v_add_u32_e32 v100, -16, v2
	s_nop 0
	v_cndmask_b32_e32 v75, v219, v75, vcc
	v_cmp_lt_i32_e32 vcc, -1, v100
	s_nop 1
	v_cndmask_b32_e32 v92, v219, v92, vcc
	v_cmp_lt_i32_e32 vcc, 31, v100
	v_subrev_u32_e32 v100, 17, v2
	s_nop 0
	v_cndmask_b32_e32 v76, v219, v76, vcc
	v_cmp_lt_i32_e32 vcc, -1, v100
	s_nop 1
	v_cndmask_b32_e32 v93, v219, v93, vcc
	v_cmp_lt_i32_e32 vcc, 31, v100
	v_subrev_u32_e32 v100, 18, v2
	s_nop 0
	v_cndmask_b32_e32 v77, v219, v77, vcc
	v_cmp_lt_i32_e32 vcc, -1, v100
	s_nop 1
	v_cndmask_b32_e32 v94, v219, v94, vcc
	v_cmp_lt_i32_e32 vcc, 31, v100
	v_subrev_u32_e32 v100, 19, v2
	s_nop 0
	v_cndmask_b32_e32 v78, v219, v78, vcc
	v_cmp_lt_i32_e32 vcc, -1, v100
	s_nop 1
	v_cndmask_b32_e32 v95, v219, v95, vcc
	v_cmp_lt_i32_e32 vcc, 31, v100
	v_subrev_u32_e32 v100, 24, v2
	s_nop 0
	v_cndmask_b32_e32 v79, v219, v79, vcc
	v_cmp_lt_i32_e32 vcc, -1, v100
	s_nop 1
	v_cndmask_b32_e32 v96, v219, v96, vcc
	v_cmp_lt_i32_e32 vcc, 31, v100
	v_subrev_u32_e32 v100, 25, v2
	s_nop 0
	v_cndmask_b32_e32 v80, v219, v80, vcc
	v_cmp_lt_i32_e32 vcc, -1, v100
	s_nop 1
	v_cndmask_b32_e32 v97, v219, v97, vcc
	v_cmp_lt_i32_e32 vcc, 31, v100
	v_subrev_u32_e32 v100, 26, v2
	v_subrev_u32_e32 v2, 27, v2
	v_cndmask_b32_e32 v81, v219, v81, vcc
	v_cmp_lt_i32_e32 vcc, -1, v100
	s_nop 1
	v_cndmask_b32_e32 v98, v219, v98, vcc
	v_cmp_lt_i32_e32 vcc, 31, v100
	s_nop 1
	v_cndmask_b32_e32 v82, v219, v82, vcc
	v_cmp_lt_i32_e32 vcc, -1, v2
	s_nop 1
	v_cndmask_b32_e32 v99, v219, v99, vcc
	v_cmp_lt_i32_e32 vcc, 31, v2
	s_nop 1
	v_cndmask_b32_e32 v83, v219, v83, vcc

.LBB0_564:
	v_add_f32_e32 v100, v84, v85
	ds_read_b64_tr_b16 v[84:85], v191 offset:0
	ds_read_b64_tr_b16 v[86:87], v191 offset:0x800
	ds_read_b64_tr_b16 v[88:89], v191 offset:0x1000
	ds_read_b64_tr_b16 v[90:91], v191 offset:0x1800
	ds_read_b64_tr_b16 v[92:93], v191 offset:0x2000
	ds_read_b64_tr_b16 v[94:95], v191 offset:0x2800
	ds_read_b64_tr_b16 v[96:97], v191 offset:0x3000
	ds_read_b64_tr_b16 v[98:99], v191 offset:0x3800
	v_fmac_f32_e32 v100, v221, v2
	s_waitcnt lgkmcnt(6)
	v_mfma_f32_32x32x16_bf16 v[52:67], v[84:87], v[68:71], v[52:67]
	ds_read_b64_tr_b16 v[84:85], v191 offset:0x200
	ds_read_b64_tr_b16 v[86:87], v191 offset:0xa00
	s_waitcnt lgkmcnt(6)
	v_mfma_f32_32x32x16_bf16 v[52:67], v[88:91], v[72:75], v[52:67]
	ds_read_b64_tr_b16 v[88:89], v191 offset:0x1200
	ds_read_b64_tr_b16 v[90:91], v191 offset:0x1a00
	s_waitcnt lgkmcnt(6)
	v_mfma_f32_32x32x16_bf16 v[52:67], v[92:95], v[76:79], v[52:67]
	ds_read_b64_tr_b16 v[92:93], v191 offset:0x2200
	ds_read_b64_tr_b16 v[94:95], v191 offset:0x2a00
	s_waitcnt lgkmcnt(6)
	v_mfma_f32_32x32x16_bf16 v[52:67], v[96:99], v[80:83], v[52:67]
	ds_read_b64_tr_b16 v[96:97], v191 offset:0x3200
	ds_read_b64_tr_b16 v[98:99], v191 offset:0x3a00
	s_waitcnt lgkmcnt(6)
	v_mfma_f32_32x32x16_bf16 v[36:51], v[84:87], v[68:71], v[36:51]
	ds_read_b64_tr_b16 v[84:85], v191 offset:0x400
	ds_read_b64_tr_b16 v[86:87], v191 offset:0xc00
	s_waitcnt lgkmcnt(6)
	v_mfma_f32_32x32x16_bf16 v[36:51], v[88:91], v[72:75], v[36:51]
	ds_read_b64_tr_b16 v[88:89], v191 offset:0x1400
	ds_read_b64_tr_b16 v[90:91], v191 offset:0x1c00
	s_waitcnt lgkmcnt(6)
	v_mfma_f32_32x32x16_bf16 v[36:51], v[92:95], v[76:79], v[36:51]
	ds_read_b64_tr_b16 v[92:93], v191 offset:0x2400
	ds_read_b64_tr_b16 v[94:95], v191 offset:0x2c00
	s_waitcnt lgkmcnt(6)
	v_mfma_f32_32x32x16_bf16 v[36:51], v[96:99], v[80:83], v[36:51]
	ds_read_b64_tr_b16 v[96:97], v191 offset:0x3400
	ds_read_b64_tr_b16 v[98:99], v191 offset:0x3c00
	s_waitcnt lgkmcnt(6)
	v_mfma_f32_32x32x16_bf16 v[20:35], v[84:87], v[68:71], v[20:35]
	ds_read_b64_tr_b16 v[84:85], v191 offset:0x600
	ds_read_b64_tr_b16 v[86:87], v191 offset:0xe00
	s_waitcnt lgkmcnt(6)
	v_mfma_f32_32x32x16_bf16 v[20:35], v[88:91], v[72:75], v[20:35]
	ds_read_b64_tr_b16 v[88:89], v191 offset:0x1600
	ds_read_b64_tr_b16 v[90:91], v191 offset:0x1e00
	s_waitcnt lgkmcnt(6)
	v_mfma_f32_32x32x16_bf16 v[20:35], v[92:95], v[76:79], v[20:35]
	ds_read_b64_tr_b16 v[92:93], v191 offset:0x2600
	ds_read_b64_tr_b16 v[94:95], v191 offset:0x2e00
	s_waitcnt lgkmcnt(6)
	v_mfma_f32_32x32x16_bf16 v[20:35], v[96:99], v[80:83], v[20:35]
	ds_read_b64_tr_b16 v[96:97], v191 offset:0x3600
	ds_read_b64_tr_b16 v[98:99], v191 offset:0x3e00
	s_waitcnt lgkmcnt(6)
	v_mfma_f32_32x32x16_bf16 v[4:19], v[84:87], v[68:71], v[4:19]
	s_waitcnt lgkmcnt(4)
	v_mfma_f32_32x32x16_bf16 v[4:19], v[88:91], v[72:75], v[4:19]
	s_waitcnt lgkmcnt(2)
	v_mfma_f32_32x32x16_bf16 v[4:19], v[92:95], v[76:79], v[4:19]
	s_waitcnt lgkmcnt(0)
	v_mfma_f32_32x32x16_bf16 v[4:19], v[96:99], v[80:83], v[4:19]
.Ltail_a0b0:
	s_setprio 0
	v_mov_b32_e32 v221, v100
	s_and_b64 vcc, exec, s[4:5]
	s_cbranch_vccz .LBB0_543
	s_branch .LBB0_544

.LBB0_571:
	s_add_i32 s98, s63, 64
	s_cmp_le_i32 s98, s28
	s_cbranch_scc0 .Lorig_a0b1
	ds_read_b128 v[116:119], v189 offset:24576
	ds_read_b128 v[120:123], v226 offset:24576
	ds_read_b128 v[124:127], v227 offset:24576
	ds_read_b128 v[128:131], v228 offset:24576
	s_waitcnt lgkmcnt(3)
	v_mfma_f32_32x32x16_bf16 v[84:99], v[116:119], v[132:135], 0
	ds_read_b128 v[116:119], v232 offset:24576
	s_waitcnt lgkmcnt(3)
	v_mfma_f32_32x32x16_bf16 v[84:99], v[120:123], v[136:139], v[84:99]
	ds_read_b128 v[120:123], v233 offset:24576
	s_waitcnt lgkmcnt(3)
	v_mfma_f32_32x32x16_bf16 v[84:99], v[124:127], v[140:143], v[84:99]
	ds_read_b128 v[124:127], v234 offset:24576
	s_waitcnt lgkmcnt(3)
	v_mfma_f32_32x32x16_bf16 v[84:99], v[128:131], v[144:147], v[84:99]
	ds_read_b128 v[128:131], v235 offset:24576
	s_waitcnt lgkmcnt(3)
	v_mfma_f32_32x32x16_bf16 v[84:99], v[116:119], v[148:151], v[84:99]
	ds_read_b128 v[116:119], v190 offset:24576
	s_waitcnt lgkmcnt(3)
	v_mfma_f32_32x32x16_bf16 v[84:99], v[120:123], v[152:155], v[84:99]
	ds_read_b128 v[120:123], v229 offset:24576
	s_waitcnt lgkmcnt(3)
	v_mfma_f32_32x32x16_bf16 v[84:99], v[124:127], v[156:159], v[84:99]
	ds_read_b128 v[124:127], v230 offset:24576
	s_waitcnt lgkmcnt(3)
	v_mfma_f32_32x32x16_bf16 v[84:99], v[128:131], v[160:163], v[84:99]
	ds_read_b128 v[128:131], v231 offset:24576
	s_waitcnt lgkmcnt(3)
	v_mfma_f32_32x32x16_bf16 v[84:99], v[116:119], v[164:167], v[84:99]
	ds_read_b128 v[116:119], v189 offset:32768
	s_waitcnt lgkmcnt(3)
	v_mfma_f32_32x32x16_bf16 v[84:99], v[120:123], v[172:175], v[84:99]
	ds_read_b128 v[120:123], v226 offset:32768
	s_waitcnt lgkmcnt(3)
	v_mfma_f32_32x32x16_bf16 v[84:99], v[124:127], v[168:171], v[84:99]
	ds_read_b128 v[124:127], v227 offset:32768
	s_waitcnt lgkmcnt(3)
	v_mfma_f32_32x32x16_bf16 v[84:99], v[128:131], v[176:179], v[84:99]
	ds_read_b128 v[128:131], v228 offset:32768
	s_waitcnt lgkmcnt(3)
	v_mfma_f32_32x32x16_bf16 v[68:83], v[116:119], v[132:135], 0
	ds_read_b128 v[116:119], v232 offset:32768
	s_waitcnt lgkmcnt(3)
	v_mfma_f32_32x32x16_bf16 v[68:83], v[120:123], v[136:139], v[68:83]
	ds_read_b128 v[120:123], v233 offset:32768
	s_waitcnt lgkmcnt(3)
	v_mfma_f32_32x32x16_bf16 v[68:83], v[124:127], v[140:143], v[68:83]
	ds_read_b128 v[124:127], v234 offset:32768
	s_waitcnt lgkmcnt(3)
	v_mfma_f32_32x32x16_bf16 v[68:83], v[128:131], v[144:147], v[68:83]
	ds_read_b128 v[128:131], v235 offset:32768
	s_waitcnt lgkmcnt(3)
	v_mfma_f32_32x32x16_bf16 v[68:83], v[116:119], v[148:151], v[68:83]
	ds_read_b128 v[116:119], v190 offset:28672
	s_waitcnt lgkmcnt(3)
	v_mfma_f32_32x32x16_bf16 v[68:83], v[120:123], v[152:155], v[68:83]
	ds_read_b128 v[120:123], v229 offset:28672
	s_waitcnt lgkmcnt(3)
	v_mfma_f32_32x32x16_bf16 v[68:83], v[124:127], v[156:159], v[68:83]
	ds_read_b128 v[124:127], v230 offset:28672
	s_waitcnt lgkmcnt(3)
	v_mfma_f32_32x32x16_bf16 v[68:83], v[128:131], v[160:163], v[68:83]
	ds_read_b128 v[128:131], v231 offset:28672
	s_waitcnt lgkmcnt(3)
	v_mfma_f32_32x32x16_bf16 v[68:83], v[116:119], v[164:167], v[68:83]
	s_waitcnt lgkmcnt(2)
	v_mfma_f32_32x32x16_bf16 v[68:83], v[120:123], v[172:175], v[68:83]
	s_waitcnt lgkmcnt(1)
	v_mfma_f32_32x32x16_bf16 v[68:83], v[124:127], v[168:171], v[68:83]
	s_waitcnt lgkmcnt(0)
	v_mfma_f32_32x32x16_bf16 v[68:83], v[128:131], v[176:179], v[68:83]
	ds_read_b64_tr_b16 v[116:117], v191 offset:16384
	ds_read_b64_tr_b16 v[118:119], v191 offset:18432
	ds_read_b64_tr_b16 v[120:121], v191 offset:20480
	ds_read_b64_tr_b16 v[122:123], v191 offset:22528
	ds_read_b64_tr_b16 v[124:125], v191 offset:16896
	ds_read_b64_tr_b16 v[126:127], v191 offset:18944
	ds_read_b64_tr_b16 v[128:129], v191 offset:20992
	ds_read_b64_tr_b16 v[130:131], v191 offset:23040
	s_nop 7
	s_nop 3
	v_max3_f32 v2, v84, v85, v86
	v_max3_f32 v251, v68, v69, v70
	v_max3_f32 v2, v2, v87, v88
	v_max3_f32 v251, v251, v71, v72
	v_max3_f32 v2, v2, v89, v90
	v_max3_f32 v251, v251, v73, v74
	v_max3_f32 v2, v2, v91, v92
	v_max3_f32 v251, v251, v75, v76
	v_max3_f32 v2, v2, v93, v94
	v_max3_f32 v251, v251, v77, v78
	v_max3_f32 v2, v2, v95, v96
	v_max3_f32 v251, v251, v79, v80
	v_max3_f32 v2, v2, v97, v98
	v_max3_f32 v251, v251, v81, v82
	v_max3_f32 v2, v2, v99, v83
	v_max_f32_e32 v2, v2, v251
	v_mov_b32_e32 v251, v2
	s_nop 1
	v_permlane32_swap_b32_e32 v2, v251
	v_max_f32_e32 v251, v251, v251
	v_max_f32_e32 v2, v2, v2
	v_max_f32_e32 v2, v2, v251
	v_sub_f32_e32 v2, v2, v222
	v_cmp_ge_f32_e32 vcc, s72, v2
	s_cmp_eq_u64 vcc, exec
	s_cbranch_scc0 .Lfb_a0b1
	v_sub_f32_e32 v100, v84, v222
	v_sub_f32_e32 v101, v85, v222
	v_sub_f32_e32 v102, v86, v222
	v_sub_f32_e32 v103, v87, v222
	v_sub_f32_e32 v104, v88, v222
	v_sub_f32_e32 v105, v89, v222
	v_sub_f32_e32 v106, v90, v222
	v_sub_f32_e32 v107, v91, v222
	v_sub_f32_e32 v108, v92, v222
	v_sub_f32_e32 v109, v93, v222
	v_sub_f32_e32 v110, v94, v222
	v_sub_f32_e32 v111, v95, v222
	v_sub_f32_e32 v112, v96, v222
	v_sub_f32_e32 v113, v97, v222
	v_sub_f32_e32 v114, v98, v222
	v_sub_f32_e32 v115, v99, v222
	v_exp_f32_e32 v100, v100
	v_exp_f32_e32 v101, v101
	v_exp_f32_e32 v102, v102
	v_exp_f32_e32 v103, v103
	v_exp_f32_e32 v104, v104
	v_exp_f32_e32 v105, v105
	v_exp_f32_e32 v106, v106
	v_exp_f32_e32 v107, v107
	v_exp_f32_e32 v108, v108
	v_exp_f32_e32 v109, v109
	v_exp_f32_e32 v110, v110
	v_exp_f32_e32 v111, v111
	v_exp_f32_e32 v112, v112
	v_exp_f32_e32 v113, v113
	v_exp_f32_e32 v114, v114
	v_exp_f32_e32 v115, v115
	v_add_f32_e32 v237, v100, v101
	v_add_f32_e32 v251, v102, v103
	v_add_f32_e32 v237, v237, v104
	v_add_f32_e32 v251, v251, v105
	v_add_f32_e32 v237, v237, v106
	v_add_f32_e32 v251, v251, v107
	v_add_f32_e32 v237, v237, v108
	v_add_f32_e32 v251, v251, v109
	v_add_f32_e32 v237, v237, v110
	v_add_f32_e32 v251, v251, v111
	v_add_f32_e32 v237, v237, v112
	v_add_f32_e32 v251, v251, v113
	v_add_f32_e32 v237, v237, v114
	v_add_f32_e32 v251, v251, v115
	v_add_f32_e32 v237, v237, v251
	v_cvt_pk_bf16_f32 v238, v100, v101
	v_cvt_pk_bf16_f32 v239, v102, v103
	v_cvt_pk_bf16_f32 v240, v104, v105
	v_cvt_pk_bf16_f32 v241, v106, v107
	v_cvt_pk_bf16_f32 v242, v108, v109
	v_cvt_pk_bf16_f32 v243, v110, v111
	v_cvt_pk_bf16_f32 v244, v112, v113
	v_cvt_pk_bf16_f32 v245, v114, v115
	s_nop 1
	v_permlane32_swap_b32_e32 v238, v240
	v_permlane32_swap_b32_e32 v239, v241
	v_permlane32_swap_b32_e32 v242, v244
	v_permlane32_swap_b32_e32 v243, v245
	v_sub_f32_e32 v100, v68, v222
	v_sub_f32_e32 v101, v69, v222
	v_sub_f32_e32 v102, v70, v222
	v_sub_f32_e32 v103, v71, v222
	v_sub_f32_e32 v104, v72, v222
	v_sub_f32_e32 v105, v73, v222
	v_sub_f32_e32 v106, v74, v222
	v_sub_f32_e32 v107, v75, v222
	v_sub_f32_e32 v108, v76, v222
	v_sub_f32_e32 v109, v77, v222
	v_sub_f32_e32 v110, v78, v222
	v_sub_f32_e32 v111, v79, v222
	v_sub_f32_e32 v112, v80, v222
	v_sub_f32_e32 v113, v81, v222
	v_sub_f32_e32 v114, v82, v222
	v_sub_f32_e32 v115, v83, v222
	v_exp_f32_e32 v100, v100
	v_exp_f32_e32 v101, v101
	v_exp_f32_e32 v102, v102
	v_exp_f32_e32 v103, v103
	v_exp_f32_e32 v104, v104
	v_exp_f32_e32 v105, v105
	v_exp_f32_e32 v106, v106
	v_exp_f32_e32 v107, v107
	v_exp_f32_e32 v108, v108
	v_exp_f32_e32 v109, v109
	v_exp_f32_e32 v110, v110
	v_exp_f32_e32 v111, v111
	v_exp_f32_e32 v112, v112
	v_exp_f32_e32 v113, v113
	v_exp_f32_e32 v114, v114
	v_exp_f32_e32 v115, v115
	v_add_f32_e32 v250, v100, v101
	v_add_f32_e32 v251, v102, v103
	v_add_f32_e32 v250, v250, v104
	v_add_f32_e32 v251, v251, v105
	v_add_f32_e32 v250, v250, v106
	v_add_f32_e32 v251, v251, v107
	v_add_f32_e32 v250, v250, v108
	v_add_f32_e32 v251, v251, v109
	v_add_f32_e32 v250, v250, v110
	v_add_f32_e32 v251, v251, v111
	v_add_f32_e32 v250, v250, v112
	v_add_f32_e32 v251, v251, v113
	v_add_f32_e32 v250, v250, v114
	v_add_f32_e32 v251, v251, v115
	v_add_f32_e32 v250, v250, v251
	v_cvt_pk_bf16_f32 v84, v100, v101
	v_cvt_pk_bf16_f32 v85, v102, v103
	v_cvt_pk_bf16_f32 v86, v104, v105
	v_cvt_pk_bf16_f32 v87, v106, v107
	v_cvt_pk_bf16_f32 v88, v108, v109
	v_cvt_pk_bf16_f32 v89, v110, v111
	v_cvt_pk_bf16_f32 v90, v112, v113
	v_cvt_pk_bf16_f32 v91, v114, v115
	s_nop 1
	v_permlane32_swap_b32_e32 v84, v86
	v_permlane32_swap_b32_e32 v85, v87
	v_permlane32_swap_b32_e32 v88, v90
	v_permlane32_swap_b32_e32 v89, v91
	v_add_f32_e32 v237, v237, v250
	v_mov_b32_e32 v250, v237
	s_nop 1
	v_permlane32_swap_b32_e32 v237, v250
	v_add_f32_e32 v237, v237, v250
	v_add_f32_e32 v100, v237, v221
	v_mov_b32_e32 v223, v222
	s_waitcnt lgkmcnt(6)
	v_mfma_f32_32x32x16_bf16 v[52:67], v[116:119], v[238:241], v[52:67]
	ds_read_b64_tr_b16 v[116:117], v191 offset:17408
	ds_read_b64_tr_b16 v[118:119], v191 offset:19456
	s_waitcnt lgkmcnt(6)
	v_mfma_f32_32x32x16_bf16 v[52:67], v[120:123], v[242:245], v[52:67]
	ds_read_b64_tr_b16 v[120:121], v191 offset:21504
	ds_read_b64_tr_b16 v[122:123], v191 offset:23552
	s_waitcnt lgkmcnt(6)
	v_mfma_f32_32x32x16_bf16 v[36:51], v[124:127], v[238:241], v[36:51]
	ds_read_b64_tr_b16 v[124:125], v191 offset:17920
	ds_read_b64_tr_b16 v[126:127], v191 offset:19968
	s_waitcnt lgkmcnt(6)
	v_mfma_f32_32x32x16_bf16 v[36:51], v[128:131], v[242:245], v[36:51]
	ds_read_b64_tr_b16 v[128:129], v191 offset:22016
	ds_read_b64_tr_b16 v[130:131], v191 offset:24064
	s_waitcnt lgkmcnt(6)
	v_mfma_f32_32x32x16_bf16 v[20:35], v[116:119], v[238:241], v[20:35]
	ds_read_b64_tr_b16 v[116:117], v191 offset:24576
	ds_read_b64_tr_b16 v[118:119], v191 offset:26624
	s_waitcnt lgkmcnt(6)
	v_mfma_f32_32x32x16_bf16 v[20:35], v[120:123], v[242:245], v[20:35]
	ds_read_b64_tr_b16 v[120:121], v191 offset:28672
	ds_read_b64_tr_b16 v[122:123], v191 offset:30720
	s_waitcnt lgkmcnt(6)
	v_mfma_f32_32x32x16_bf16 v[4:19], v[124:127], v[238:241], v[4:19]
	ds_read_b64_tr_b16 v[124:125], v191 offset:25088
	ds_read_b64_tr_b16 v[126:127], v191 offset:27136
	s_waitcnt lgkmcnt(6)
	v_mfma_f32_32x32x16_bf16 v[4:19], v[128:131], v[242:245], v[4:19]
	ds_read_b64_tr_b16 v[128:129], v191 offset:29184
	ds_read_b64_tr_b16 v[130:131], v191 offset:31232
	s_nop 1
	s_waitcnt lgkmcnt(6)
	v_mfma_f32_32x32x16_bf16 v[52:67], v[116:119], v[84:87], v[52:67]
	ds_read_b64_tr_b16 v[116:117], v191 offset:25600
	ds_read_b64_tr_b16 v[118:119], v191 offset:27648
	s_waitcnt lgkmcnt(6)
	v_mfma_f32_32x32x16_bf16 v[52:67], v[120:123], v[88:91], v[52:67]
	ds_read_b64_tr_b16 v[120:121], v191 offset:29696
	ds_read_b64_tr_b16 v[122:123], v191 offset:31744
	s_waitcnt lgkmcnt(6)
	v_mfma_f32_32x32x16_bf16 v[36:51], v[124:127], v[84:87], v[36:51]
	ds_read_b64_tr_b16 v[124:125], v191 offset:26112
	ds_read_b64_tr_b16 v[126:127], v191 offset:28160
	s_waitcnt lgkmcnt(6)
	v_mfma_f32_32x32x16_bf16 v[36:51], v[128:131], v[88:91], v[36:51]
	ds_read_b64_tr_b16 v[128:129], v191 offset:30208
	ds_read_b64_tr_b16 v[130:131], v191 offset:32256
	s_waitcnt lgkmcnt(6)
	v_mfma_f32_32x32x16_bf16 v[20:35], v[116:119], v[84:87], v[20:35]
	s_waitcnt lgkmcnt(4)
	v_mfma_f32_32x32x16_bf16 v[20:35], v[120:123], v[88:91], v[20:35]
	s_waitcnt lgkmcnt(2)
	v_mfma_f32_32x32x16_bf16 v[4:19], v[124:127], v[84:87], v[4:19]
	s_waitcnt lgkmcnt(0)
	v_mfma_f32_32x32x16_bf16 v[4:19], v[128:131], v[88:91], v[4:19]
	s_branch .Ltail_a0b1

.Lorig_a0b1:
	ds_read_b128 v[100:103], v189 offset:24576
	ds_read_b128 v[104:107], v189 offset:32768
	ds_read_b128 v[108:111], v226 offset:24576
	ds_read_b128 v[112:115], v226 offset:32768
	ds_read_b128 v[116:119], v227 offset:24576
	ds_read_b128 v[120:123], v227 offset:32768
	ds_read_b128 v[124:127], v228 offset:24576
	ds_read_b128 v[128:131], v228 offset:32768
	s_waitcnt lgkmcnt(7)
	v_mfma_f32_32x32x16_bf16 v[84:99], v[100:103], v[132:135], 0
	ds_read_b128 v[100:103], v232 offset:24576
	s_waitcnt lgkmcnt(7)
	v_mfma_f32_32x32x16_bf16 v[68:83], v[104:107], v[132:135], 0
	ds_read_b128 v[104:107], v232 offset:32768
	s_waitcnt lgkmcnt(7)
	v_mfma_f32_32x32x16_bf16 v[84:99], v[108:111], v[136:139], v[84:99]
	ds_read_b128 v[108:111], v233 offset:24576
	s_waitcnt lgkmcnt(7)
	v_mfma_f32_32x32x16_bf16 v[68:83], v[112:115], v[136:139], v[68:83]
	ds_read_b128 v[112:115], v233 offset:32768
	s_waitcnt lgkmcnt(7)
	v_mfma_f32_32x32x16_bf16 v[84:99], v[116:119], v[140:143], v[84:99]
	ds_read_b128 v[116:119], v234 offset:24576
	s_waitcnt lgkmcnt(7)
	v_mfma_f32_32x32x16_bf16 v[68:83], v[120:123], v[140:143], v[68:83]
	ds_read_b128 v[120:123], v234 offset:32768
	s_waitcnt lgkmcnt(7)
	v_mfma_f32_32x32x16_bf16 v[84:99], v[124:127], v[144:147], v[84:99]
	ds_read_b128 v[124:127], v235 offset:24576
	s_waitcnt lgkmcnt(7)
	v_mfma_f32_32x32x16_bf16 v[68:83], v[128:131], v[144:147], v[68:83]
	ds_read_b128 v[128:131], v235 offset:32768
	s_waitcnt lgkmcnt(7)
	v_mfma_f32_32x32x16_bf16 v[84:99], v[100:103], v[148:151], v[84:99]
	ds_read_b128 v[100:103], v190 offset:24576
	s_waitcnt lgkmcnt(7)
	v_mfma_f32_32x32x16_bf16 v[68:83], v[104:107], v[148:151], v[68:83]
	ds_read_b128 v[104:107], v190 offset:28672
	s_waitcnt lgkmcnt(7)
	v_mfma_f32_32x32x16_bf16 v[84:99], v[108:111], v[152:155], v[84:99]
	ds_read_b128 v[108:111], v229 offset:24576
	s_waitcnt lgkmcnt(7)
	v_mfma_f32_32x32x16_bf16 v[68:83], v[112:115], v[152:155], v[68:83]
	ds_read_b128 v[112:115], v229 offset:28672
	s_waitcnt lgkmcnt(7)
	v_mfma_f32_32x32x16_bf16 v[84:99], v[116:119], v[156:159], v[84:99]
	ds_read_b128 v[116:119], v230 offset:24576
	s_waitcnt lgkmcnt(7)
	v_mfma_f32_32x32x16_bf16 v[68:83], v[120:123], v[156:159], v[68:83]
	ds_read_b128 v[120:123], v230 offset:28672
	s_waitcnt lgkmcnt(7)
	v_mfma_f32_32x32x16_bf16 v[84:99], v[124:127], v[160:163], v[84:99]
	ds_read_b128 v[124:127], v231 offset:24576
	s_waitcnt lgkmcnt(7)
	v_mfma_f32_32x32x16_bf16 v[68:83], v[128:131], v[160:163], v[68:83]
	ds_read_b128 v[128:131], v231 offset:28672
	s_waitcnt lgkmcnt(7)
	v_mfma_f32_32x32x16_bf16 v[84:99], v[100:103], v[164:167], v[84:99]
	s_waitcnt lgkmcnt(6)
	v_mfma_f32_32x32x16_bf16 v[68:83], v[104:107], v[164:167], v[68:83]
	s_waitcnt lgkmcnt(5)
	v_mfma_f32_32x32x16_bf16 v[84:99], v[108:111], v[172:175], v[84:99]
	s_waitcnt lgkmcnt(4)
	v_mfma_f32_32x32x16_bf16 v[68:83], v[112:115], v[172:175], v[68:83]
	s_waitcnt lgkmcnt(3)
	v_mfma_f32_32x32x16_bf16 v[84:99], v[116:119], v[168:171], v[84:99]
	s_waitcnt lgkmcnt(2)
	v_mfma_f32_32x32x16_bf16 v[68:83], v[120:123], v[168:171], v[68:83]
	s_waitcnt lgkmcnt(1)
	v_mfma_f32_32x32x16_bf16 v[84:99], v[124:127], v[176:179], v[84:99]
	s_waitcnt lgkmcnt(0)
	v_mfma_f32_32x32x16_bf16 v[68:83], v[128:131], v[176:179], v[68:83]
	s_nop 0
	s_add_i32 s6, s63, 64
	s_cmp_le_i32 s6, s28
	s_cbranch_scc1 .LBB0_573
	v_add_u32_e32 v2, s17, v220
	v_subrev_u32_e32 v100, 64, v2
	v_cmp_lt_i32_e32 vcc, -1, v100
	s_nop 2
	v_cndmask_b32_e32 v84, v219, v84, vcc
	v_cmp_lt_i32_e32 vcc, 31, v100
	v_add_u32_e32 v100, 0xffffffbf, v2
	s_nop 0
	v_cndmask_b32_e32 v68, v219, v68, vcc
	v_cmp_lt_i32_e32 vcc, -1, v100
	s_nop 1
	v_cndmask_b32_e32 v85, v219, v85, vcc
	v_cmp_lt_i32_e32 vcc, 31, v100
	v_add_u32_e32 v100, 0xffffffbe, v2
	s_nop 0
	v_cndmask_b32_e32 v69, v219, v69, vcc
	v_cmp_lt_i32_e32 vcc, -1, v100
	s_nop 1
	v_cndmask_b32_e32 v86, v219, v86, vcc
	v_cmp_lt_i32_e32 vcc, 31, v100
	v_add_u32_e32 v100, 0xffffffbd, v2
	s_nop 0
	v_cndmask_b32_e32 v70, v219, v70, vcc
	v_cmp_lt_i32_e32 vcc, -1, v100
	s_nop 1
	v_cndmask_b32_e32 v87, v219, v87, vcc
	v_cmp_lt_i32_e32 vcc, 31, v100
	v_add_u32_e32 v100, 0xffffffb8, v2
	s_nop 0
	v_cndmask_b32_e32 v71, v219, v71, vcc
	v_cmp_lt_i32_e32 vcc, -1, v100
	s_nop 1
	v_cndmask_b32_e32 v88, v219, v88, vcc
	v_cmp_lt_i32_e32 vcc, 31, v100
	v_add_u32_e32 v100, 0xffffffb7, v2
	s_nop 0
	v_cndmask_b32_e32 v72, v219, v72, vcc
	v_cmp_lt_i32_e32 vcc, -1, v100
	s_nop 1
	v_cndmask_b32_e32 v89, v219, v89, vcc
	v_cmp_lt_i32_e32 vcc, 31, v100
	v_add_u32_e32 v100, 0xffffffb6, v2
	s_nop 0
	v_cndmask_b32_e32 v73, v219, v73, vcc
	v_cmp_lt_i32_e32 vcc, -1, v100
	s_nop 1
	v_cndmask_b32_e32 v90, v219, v90, vcc
	v_cmp_lt_i32_e32 vcc, 31, v100
	v_add_u32_e32 v100, 0xffffffb5, v2
	s_nop 0
	v_cndmask_b32_e32 v74, v219, v74, vcc
	v_cmp_lt_i32_e32 vcc, -1, v100
	s_nop 1
	v_cndmask_b32_e32 v91, v219, v91, vcc
	v_cmp_lt_i32_e32 vcc, 31, v100
	v_add_u32_e32 v100, 0xffffffb0, v2
	s_nop 0
	v_cndmask_b32_e32 v75, v219, v75, vcc
	v_cmp_lt_i32_e32 vcc, -1, v100
	s_nop 1
	v_cndmask_b32_e32 v92, v219, v92, vcc
	v_cmp_lt_i32_e32 vcc, 31, v100
	v_add_u32_e32 v100, 0xffffffaf, v2
	s_nop 0
	v_cndmask_b32_e32 v76, v219, v76, vcc
	v_cmp_lt_i32_e32 vcc, -1, v100
	s_nop 1
	v_cndmask_b32_e32 v93, v219, v93, vcc
	v_cmp_lt_i32_e32 vcc, 31, v100
	v_add_u32_e32 v100, 0xffffffae, v2
	s_nop 0
	v_cndmask_b32_e32 v77, v219, v77, vcc
	v_cmp_lt_i32_e32 vcc, -1, v100
	s_nop 1
	v_cndmask_b32_e32 v94, v219, v94, vcc
	v_cmp_lt_i32_e32 vcc, 31, v100
	v_add_u32_e32 v100, 0xffffffad, v2
	s_nop 0
	v_cndmask_b32_e32 v78, v219, v78, vcc
	v_cmp_lt_i32_e32 vcc, -1, v100
	s_nop 1
	v_cndmask_b32_e32 v95, v219, v95, vcc
	v_cmp_lt_i32_e32 vcc, 31, v100
	v_add_u32_e32 v100, 0xffffffa8, v2
	s_nop 0
	v_cndmask_b32_e32 v79, v219, v79, vcc
	v_cmp_lt_i32_e32 vcc, -1, v100
	s_nop 1
	v_cndmask_b32_e32 v96, v219, v96, vcc
	v_cmp_lt_i32_e32 vcc, 31, v100
	v_add_u32_e32 v100, 0xffffffa7, v2
	s_nop 0
	v_cndmask_b32_e32 v80, v219, v80, vcc
	v_cmp_lt_i32_e32 vcc, -1, v100
	s_nop 1
	v_cndmask_b32_e32 v97, v219, v97, vcc
	v_cmp_lt_i32_e32 vcc, 31, v100
	v_add_u32_e32 v100, 0xffffffa6, v2
	v_add_u32_e32 v2, 0xffffffa5, v2
	v_cndmask_b32_e32 v81, v219, v81, vcc
	v_cmp_lt_i32_e32 vcc, -1, v100
	s_nop 1
	v_cndmask_b32_e32 v98, v219, v98, vcc
	v_cmp_lt_i32_e32 vcc, 31, v100
	s_nop 1
	v_cndmask_b32_e32 v82, v219, v82, vcc
	v_cmp_lt_i32_e32 vcc, -1, v2
	s_nop 1
	v_cndmask_b32_e32 v99, v219, v99, vcc
	v_cmp_lt_i32_e32 vcc, 31, v2
	s_nop 1
	v_cndmask_b32_e32 v83, v219, v83, vcc

.LBB0_579:
	v_add_f32_e32 v100, v84, v85
	ds_read_b64_tr_b16 v[84:85], v191 offset:0x4000
	ds_read_b64_tr_b16 v[86:87], v191 offset:0x4800
	ds_read_b64_tr_b16 v[88:89], v191 offset:0x5000
	ds_read_b64_tr_b16 v[90:91], v191 offset:0x5800
	ds_read_b64_tr_b16 v[92:93], v191 offset:0x6000
	ds_read_b64_tr_b16 v[94:95], v191 offset:0x6800
	ds_read_b64_tr_b16 v[96:97], v191 offset:0x7000
	ds_read_b64_tr_b16 v[98:99], v191 offset:0x7800
	v_fmac_f32_e32 v100, v221, v2
	s_waitcnt lgkmcnt(6)
	v_mfma_f32_32x32x16_bf16 v[52:67], v[84:87], v[68:71], v[52:67]
	ds_read_b64_tr_b16 v[84:85], v191 offset:0x4200
	ds_read_b64_tr_b16 v[86:87], v191 offset:0x4a00
	s_waitcnt lgkmcnt(6)
	v_mfma_f32_32x32x16_bf16 v[52:67], v[88:91], v[72:75], v[52:67]
	ds_read_b64_tr_b16 v[88:89], v191 offset:0x5200
	ds_read_b64_tr_b16 v[90:91], v191 offset:0x5a00
	s_waitcnt lgkmcnt(6)
	v_mfma_f32_32x32x16_bf16 v[52:67], v[92:95], v[76:79], v[52:67]
	ds_read_b64_tr_b16 v[92:93], v191 offset:0x6200
	ds_read_b64_tr_b16 v[94:95], v191 offset:0x6a00
	s_waitcnt lgkmcnt(6)
	v_mfma_f32_32x32x16_bf16 v[52:67], v[96:99], v[80:83], v[52:67]
	ds_read_b64_tr_b16 v[96:97], v191 offset:0x7200
	ds_read_b64_tr_b16 v[98:99], v191 offset:0x7a00
	s_waitcnt lgkmcnt(6)
	v_mfma_f32_32x32x16_bf16 v[36:51], v[84:87], v[68:71], v[36:51]
	ds_read_b64_tr_b16 v[84:85], v191 offset:0x4400
	ds_read_b64_tr_b16 v[86:87], v191 offset:0x4c00
	s_waitcnt lgkmcnt(6)
	v_mfma_f32_32x32x16_bf16 v[36:51], v[88:91], v[72:75], v[36:51]
	ds_read_b64_tr_b16 v[88:89], v191 offset:0x5400
	ds_read_b64_tr_b16 v[90:91], v191 offset:0x5c00
	s_waitcnt lgkmcnt(6)
	v_mfma_f32_32x32x16_bf16 v[36:51], v[92:95], v[76:79], v[36:51]
	ds_read_b64_tr_b16 v[92:93], v191 offset:0x6400
	ds_read_b64_tr_b16 v[94:95], v191 offset:0x6c00
	s_waitcnt lgkmcnt(6)
	v_mfma_f32_32x32x16_bf16 v[36:51], v[96:99], v[80:83], v[36:51]
	ds_read_b64_tr_b16 v[96:97], v191 offset:0x7400
	ds_read_b64_tr_b16 v[98:99], v191 offset:0x7c00
	s_waitcnt lgkmcnt(6)
	v_mfma_f32_32x32x16_bf16 v[20:35], v[84:87], v[68:71], v[20:35]
	ds_read_b64_tr_b16 v[84:85], v191 offset:0x4600
	ds_read_b64_tr_b16 v[86:87], v191 offset:0x4e00
	s_waitcnt lgkmcnt(6)
	v_mfma_f32_32x32x16_bf16 v[20:35], v[88:91], v[72:75], v[20:35]
	ds_read_b64_tr_b16 v[88:89], v191 offset:0x5600
	ds_read_b64_tr_b16 v[90:91], v191 offset:0x5e00
	s_waitcnt lgkmcnt(6)
	v_mfma_f32_32x32x16_bf16 v[20:35], v[92:95], v[76:79], v[20:35]
	ds_read_b64_tr_b16 v[92:93], v191 offset:0x6600
	ds_read_b64_tr_b16 v[94:95], v191 offset:0x6e00
	s_waitcnt lgkmcnt(6)
	v_mfma_f32_32x32x16_bf16 v[20:35], v[96:99], v[80:83], v[20:35]
	ds_read_b64_tr_b16 v[96:97], v191 offset:0x7600
	ds_read_b64_tr_b16 v[98:99], v191 offset:0x7e00
	s_waitcnt lgkmcnt(6)
	v_mfma_f32_32x32x16_bf16 v[4:19], v[84:87], v[68:71], v[4:19]
	s_waitcnt lgkmcnt(4)
	v_mfma_f32_32x32x16_bf16 v[4:19], v[88:91], v[72:75], v[4:19]
	s_waitcnt lgkmcnt(2)
	v_mfma_f32_32x32x16_bf16 v[4:19], v[92:95], v[76:79], v[4:19]
	s_waitcnt lgkmcnt(0)
	v_mfma_f32_32x32x16_bf16 v[4:19], v[96:99], v[80:83], v[4:19]
.Ltail_a0b1:
	s_setprio 0
	v_mov_b32_e32 v221, v100
	s_branch .LBB0_533

; #define LAS __attribute__((address_space(3)))
; #define INF(i) ((const float*)arg_ptr(i))
; __device__ __forceinline__ int v_rd_base(int lane) { return ((lane & 3) << 3) | (((lane >> 2) & 3) << 6) | (((lane >> 4) & 1) << 5) | (((lane >> 5) & 1) << 8); }
; template <int layer>
; __device__ __forceinline__ void attn_phase(LAS unsigned char* lds) {
;     ...
;     const int wid = __builtin_amdgcn_readfirstlane(tid >> 6), r32 = lane & 31, hi = lane >> 5;
;     auto koff_n = [](int tk, int j) { const int ci = j * 256 + tk, row = ci >> 4, pc = ci & 15, lc = pc ^ (row & 7); return (unsigned)(row * KLD + lc * 8) * 2u; };
;     auto koff_r = [](int tk, int j) { const int ci = j * 256 + tk, row = ci >> 3, pc = ci & 7, lc = pc ^ (row & 7); return (unsigned)(row * 64 + lc * 8) * 2u; };
;     auto voff_f = [](int tk, int j) { const int ci = j * 256 + tk, st = ci >> 5, w = ci & 31, kk = (st >> 2) * 8 + (w >> 2), key = (kk & ~0xC) | ((kk & 4) << 1) | ((kk & 8) >> 1), c = (st & 3) * 32 + (w & 3) * 8;
;         return (unsigned)(key * KLD + c) * 2u; };
;     const int tkp = (tid - 256) & 255; const unsigned kof0 = koff_n(tkp, 0), vof0 = voff_f(tkp, 0), rof0 = koff_r(tkp, 0);
;     const int kbn = r32 * 256 + ((hi * 16) ^ ((r32 & 7) << 4)), kbr0 = 16384 + r32 * 128 + ((hi * 16) ^ ((r32 & 7) << 4));
;     const unsigned ldsb = (unsigned)(uintptr_t)lds;
;     const int vb0 = (int)(unsigned)(uintptr_t)(lds + OFF_V) + v_rd_base(lane);
;     LAS float* wsl = (LAS float*)(lds + OFF_WS) + wid * 64; LAS float* li_l = wsl; LAS float* al_l = wsl + 32;
;     const float* cv_wgu = INF(layer == 0 ? 15 : 27); const float* cv_wdn = INF(layer == 0 ? 16 : 28); bf16* cv_gut = WSP(bf16, CV_MODE >= 2 ? WS_Q : WS_W_GUT); bf16* cv_dt = WSP(bf16, CV_MODE >= 2 ? WS_Q : WS_W_DT);
;     constexpr int CV_IG = 32 * 32, CV_ID = 8 * 64, CV_NIT = NEXP * (CV_IG + CV_ID);
;     int cv_it = (CV_MODE == 1) ? CV_NIT : bx * 4 + wid, cv_pend = -1; const int cv_stride = G * 4;
;     const unsigned cv_lds = (unsigned)(uintptr_t)(lds + OFF_CV) + (unsigned)(wid & 3) * 16384u;
.LBB0_1417:
	s_or_b64 exec, exec, s[4:5]
	s_mov_b32 s0, 30
	s_waitcnt lgkmcnt(0)
	s_barrier
	s_ashr_i32 s1, s0, 31
	s_lshl_b64 s[0:1], s[0:1], 3
	s_add_u32 s0, s80, s0
	s_addc_u32 s1, s81, s1
	s_load_dwordx2 s[4:5], s[0:1], 0x0
	v_mov_b32_e32 v4, v0
	s_mov_b32 s2, s78
	s_mov_b32 s9, s79
	s_mov_b32 s6, 20
	s_mov_b32 s0, 1
	s_mov_b32 s17, 0
	v_readfirstlane_b32 s0, v4
	s_ashr_i32 s3, s0, 6
	s_mov_b32 s0, 27
	s_ashr_i32 s1, s0, 31
	s_lshl_b64 s[0:1], s[0:1], 3
	s_add_u32 s0, s80, s0
	s_addc_u32 s1, s81, s1
	s_load_dwordx2 s[12:13], s[0:1], 0x0
	s_mov_b32 s0, 28
	s_ashr_i32 s1, s0, 31
	s_lshl_b64 s[0:1], s[0:1], 3
	s_add_u32 s0, s80, s0
	s_addc_u32 s1, s81, s1
	s_waitcnt lgkmcnt(0)
	s_add_u32 s60, s4, 0x3e00000
	s_addc_u32 s61, s5, 0
	s_add_u32 s62, s4, 0x13e00000
	s_load_dwordx2 s[14:15], s[0:1], 0x0
	s_addc_u32 s63, s5, 0
	s_lshl_b32 s0, s9, 2
	s_add_i32 s73, s3, s0
	s_lshl_b32 s0, s3, 14
	s_and_b32 s0, s0, 0xc000
	s_add_i32 s10, s0, 0
	s_lshl_b32 s64, s2, 2
	s_add_i32 s65, s10, 0x15000
	s_cmpk_gt_i32 s9, 0x1ff
	s_mov_b32 s70, -1
	v_writelane_b32 v252, s2, 9
	s_cbranch_scc1 .LBB0_1477
	s_add_u32 s18, s4, 0x1fe00000
	s_addc_u32 s19, s5, 0
	v_lshrrev_b32_e32 v1, 4, v4
	v_and_b32_e32 v2, 15, v4
	s_add_u32 s0, s4, 0x42000000
	v_bitop3_b32 v1, v1, v2, 15 bitop3:0x6c
	v_lshlrev_b32_e32 v2, 10, v4
	v_writelane_b32 v252, s0, 13
	s_addc_u32 s0, s5, 0
	s_ashr_i32 s7, s6, 31
	v_and_b32_e32 v2, 0x3c000, v2
	v_writelane_b32 v252, s0, 14
	s_lshl_b64 s[0:1], s[6:7], 3
	v_lshl_or_b32 v1, v1, 4, v2
	v_lshrrev_b32_e32 v2, 5, v4
	v_lshrrev_b32_e32 v5, 1, v4
	s_add_u32 s0, s80, s0
	v_and_b32_e32 v2, 4, v2
	v_bfe_u32 v3, v4, 2, 2
	v_and_b32_e32 v5, 8, v5
	s_addc_u32 s1, s81, s1
	v_or3_b32 v2, v3, v5, v2
	v_and_b32_e32 v3, 0x60, v4
	v_lshlrev_b32_e32 v5, 3, v4
	s_add_u32 s2, s4, 0x5e200000
	v_and_or_b32 v3, v5, 24, v3
	v_writelane_b32 v252, s2, 15
	s_addc_u32 s2, s5, 0
	v_bfe_u32 v7, v4, 5, 1
	v_lshlrev_b32_e32 v3, 1, v3
	s_lshl_b32 s6, s3, 5
	v_and_b32_e32 v132, 31, v4
	v_lshl_or_b32 v133, v2, 14, v3
	v_bitop3_b32 v2, v7, v4, 15 bitop3:0x78
	s_cmp_gt_i32 s3, 3
	v_writelane_b32 v252, s2, 16
	v_lshlrev_b32_e32 v2, 4, v2
	v_lshlrev_b32_e32 v3, 7, v132
	s_movk_i32 s2, 0x4000
	s_cselect_b64 s[20:21], -1, 0
	s_lshl_b32 s76, s3, 10
	v_and_b32_e32 v6, 63, v4
	s_load_dwordx2 s[0:1], s[0:1], 0x0
	v_or3_b32 v173, v2, v3, s2
	v_lshlrev_b32_e32 v3, 4, v4
	s_add_i32 s76, s76, 0
	v_lshl_or_b32 v172, v132, 8, v2
	v_xor_b32_e32 v206, 32, v172
	v_xor_b32_e32 v207, 64, v172
	v_xor_b32_e32 v237, 0x60, v172
	v_xor_b32_e32 v244, 0x80, v172
	v_xor_b32_e32 v245, 0xa0, v172
	v_xor_b32_e32 v246, 0xc0, v172
	v_xor_b32_e32 v247, 0xe0, v172
	v_lshlrev_b32_e32 v2, 3, v6
	v_and_b32_e32 v3, 0xc0, v3
	v_lshlrev_b32_e32 v5, 1, v4
	s_add_i32 s77, s76, 0x7000
	s_add_i32 s78, s76, 0xfffff000
	v_and_or_b32 v3, v2, 24, v3
	v_and_b32_e32 v5, 32, v5
	v_and_b32_e32 v2, 0x100, v2
	s_cmp_eq_u32 s3, 4
	v_or3_b32 v2, v3, v5, v2
	v_mov_b32_e32 v3, 0
	v_writelane_b32 v252, s18, 26
	s_cselect_b64 s[4:5], -1, 0
	s_add_i32 s79, s76, 0xb000
	s_add_i32 s80, s76, 0x3000
	v_writelane_b32 v252, s19, 27
	v_and_b32_e32 v4, 32, v4
	v_mov_b32_e32 v5, v3
	s_cmp_lt_i32 s3, 4
	v_add_u32_e32 v174, 0, v2
	v_lshlrev_b32_e32 v2, 4, v7
	s_waitcnt lgkmcnt(0)
	v_lshl_add_u64 v[136:137], s[0:1], 0, v[4:5]
	v_writelane_b32 v252, s3, 18
	s_cselect_b64 s[24:25], -1, 0
	s_add_i32 s81, 0, 0x10800
	v_mul_i32_i24_e32 v4, -4, v7
	s_add_i32 s83, 0, 0x10900
	s_movk_i32 s74, 0x60
	v_lshl_add_u64 v[134:135], s[18:19], 0, v[2:3]
	v_lshlrev_b32_e32 v175, 2, v6
	v_add_u32_e32 v176, s81, v2
	s_add_i32 s82, s10, 0x17000
	v_add_u32_e32 v177, s83, v2
	v_or_b32_e32 v178, 0x40000, v1
	s_add_i32 s84, s76, 0x8000
	v_or_b32_e32 v179, 0x80000, v1
	s_add_i32 s85, s76, 0x9000
	v_or_b32_e32 v180, 0xc0000, v1
	s_add_i32 s86, s76, 0xa000
	v_or_b32_e32 v181, 0x40000, v133
	v_or_b32_e32 v182, 0x80000, v133
	s_add_i32 s87, s76, 0x1000
	v_or_b32_e32 v183, 0xc0000, v133
	s_add_i32 s88, s76, 0x2000
	s_add_i32 s89, s76, 0xc000
	s_add_i32 s90, s76, 0xd000
	s_add_i32 s91, s76, 0xe000
	s_add_i32 s92, s76, 0x4000
	s_add_i32 s93, s76, 0x5000
	s_add_i32 s94, s76, 0x6000
	s_add_i32 s95, s10, 0x15400
	s_add_i32 s96, s10, 0x15800
	s_add_i32 s97, s10, 0x15c00
	s_add_i32 s30, s10, 0x16000
	s_add_i32 s31, s10, 0x16400
	s_add_i32 s22, s10, 0x16800
	s_add_i32 s23, s10, 0x16c00
	s_add_i32 s28, s10, 0x17400
	s_add_i32 s29, s10, 0x17800
	s_add_i32 s33, s10, 0x17c00
	s_add_i32 s3, s10, 0x18000
	s_add_i32 s2, s10, 0x18400
	s_add_i32 s67, s10, 0x18800
	v_writelane_b32 v252, s10, 17
	s_add_i32 s66, s10, 0x18c00
	v_add3_u32 v184, v4, s6, v132
	v_mov_b32_e32 v185, 0x358637bd
	v_cndmask_b32_e64 v186, 0, 1, s[20:21]
	s_movk_i32 s1, 0x3ff
	s_movk_i32 s0, 0x70
	s_movk_i32 s26, 0x50
	s_mov_b32 s27, 0x42800000
	v_cndmask_b32_e64 v187, 0, 1, s[4:5]
	v_mov_b32_e32 v188, 0x10000
	v_mov_b32_e32 v189, 0xff800000
	v_writelane_b32 v252, s6, 23
	s_branch .LBB0_1420

.LBB0_1452:
	ds_read_b128 v[208:211], v172 offset:32768
	ds_read_b128 v[212:215], v172 offset:40960
	ds_read_b128 v[216:219], v206 offset:32768
	ds_read_b128 v[220:223], v206 offset:40960
	ds_read_b128 v[224:227], v207 offset:32768
	ds_read_b128 v[228:231], v207 offset:40960
	ds_read_b128 v[232:235], v237 offset:32768
	ds_read_b128 v[238:241], v237 offset:40960
	s_waitcnt lgkmcnt(7)
	v_mfma_f32_32x32x16_bf16 v[84:99], v[208:211], v[100:103], 0
	ds_read_b128 v[208:211], v244 offset:32768
	s_waitcnt lgkmcnt(7)
	v_mfma_f32_32x32x16_bf16 v[68:83], v[212:215], v[100:103], 0
	ds_read_b128 v[212:215], v244 offset:40960
	s_waitcnt lgkmcnt(7)
	v_mfma_f32_32x32x16_bf16 v[84:99], v[216:219], v[104:107], v[84:99]
	ds_read_b128 v[216:219], v245 offset:32768
	s_waitcnt lgkmcnt(7)
	v_mfma_f32_32x32x16_bf16 v[68:83], v[220:223], v[104:107], v[68:83]
	ds_read_b128 v[220:223], v245 offset:40960
	s_waitcnt lgkmcnt(7)
	v_mfma_f32_32x32x16_bf16 v[84:99], v[224:227], v[108:111], v[84:99]
	ds_read_b128 v[224:227], v246 offset:32768
	s_waitcnt lgkmcnt(7)
	v_mfma_f32_32x32x16_bf16 v[68:83], v[228:231], v[108:111], v[68:83]
	ds_read_b128 v[228:231], v246 offset:40960
	s_waitcnt lgkmcnt(7)
	v_mfma_f32_32x32x16_bf16 v[84:99], v[232:235], v[112:115], v[84:99]
	ds_read_b128 v[232:235], v247 offset:32768
	s_waitcnt lgkmcnt(7)
	v_mfma_f32_32x32x16_bf16 v[68:83], v[238:241], v[112:115], v[68:83]
	ds_read_b128 v[238:241], v247 offset:40960
	s_waitcnt lgkmcnt(7)
	v_mfma_f32_32x32x16_bf16 v[84:99], v[208:211], v[116:119], v[84:99]
	s_waitcnt lgkmcnt(6)
	v_mfma_f32_32x32x16_bf16 v[68:83], v[212:215], v[116:119], v[68:83]
	s_waitcnt lgkmcnt(5)
	v_mfma_f32_32x32x16_bf16 v[84:99], v[216:219], v[120:123], v[84:99]
	s_waitcnt lgkmcnt(4)
	v_mfma_f32_32x32x16_bf16 v[68:83], v[220:223], v[120:123], v[68:83]
	s_waitcnt lgkmcnt(3)
	v_mfma_f32_32x32x16_bf16 v[84:99], v[224:227], v[124:127], v[84:99]
	s_waitcnt lgkmcnt(2)
	v_mfma_f32_32x32x16_bf16 v[68:83], v[228:231], v[124:127], v[68:83]
	s_waitcnt lgkmcnt(1)
	v_mfma_f32_32x32x16_bf16 v[84:99], v[232:235], v[128:131], v[84:99]
	s_waitcnt lgkmcnt(0)
	v_mfma_f32_32x32x16_bf16 v[68:83], v[238:241], v[128:131], v[68:83]
	ds_read_b128 v[156:159], v176
	ds_read_b128 v[194:197], v176 offset:128
	ds_read_b128 v[140:143], v176 offset:32
	ds_read_b128 v[168:171], v176 offset:160
	ds_read_b128 v[144:147], v176 offset:64
	ds_read_b128 v[198:201], v176 offset:192
	ds_read_b128 v[162:165], v176 offset:96
	ds_read_b128 v[202:205], v176 offset:224
	s_waitcnt lgkmcnt(3)
	v_pk_add_f32 v[144:145], v[92:93], v[144:145]
	v_pk_add_f32 v[150:151], v[90:91], v[142:143]
	v_pk_add_f32 v[154:155], v[88:89], v[140:141]
	v_pk_add_f32 v[160:161], v[86:87], v[158:159]
	v_pk_add_f32 v[146:147], v[94:95], v[146:147]
	s_waitcnt lgkmcnt(1)
	v_pk_add_f32 v[142:143], v[96:97], v[162:163]
	v_pk_add_f32 v[140:141], v[98:99], v[164:165]
	v_pk_add_f32 v[166:167], v[84:85], v[156:157]
	v_pk_add_f32 v[156:157], v[76:77], v[198:199]
	v_pk_add_f32 v[162:163], v[74:75], v[170:171]
	v_pk_add_f32 v[164:165], v[72:73], v[168:169]
	v_pk_add_f32 v[168:169], v[70:71], v[196:197]
	v_pk_add_f32 v[158:159], v[78:79], v[200:201]
	s_waitcnt lgkmcnt(0)
	v_pk_add_f32 v[152:153], v[80:81], v[202:203]
	v_pk_add_f32 v[148:149], v[82:83], v[204:205]
	v_pk_add_f32 v[170:171], v[68:69], v[194:195]
	s_cmp_le_i32 s18, s40
	s_cbranch_scc1 .LBB0_1454
	v_add_u32_e32 v2, s71, v190
	v_cmp_lt_i32_e32 vcc, -1, v2
	v_add_u32_e32 v68, -1, v2
	s_nop 0
	v_cndmask_b32_e32 v166, v189, v166, vcc
	v_cmp_lt_i32_e32 vcc, 31, v2
	s_nop 1
	v_cndmask_b32_e32 v170, v189, v170, vcc
	v_cmp_lt_i32_e32 vcc, -1, v68
	s_nop 1
	v_cndmask_b32_e32 v167, v189, v167, vcc
	v_cmp_lt_i32_e32 vcc, 31, v68
	v_add_u32_e32 v68, -2, v2
	s_nop 0
	v_cndmask_b32_e32 v171, v189, v171, vcc
	v_cmp_lt_i32_e32 vcc, -1, v68
	s_nop 1
	v_cndmask_b32_e32 v160, v189, v160, vcc
	v_cmp_lt_i32_e32 vcc, 31, v68
	v_add_u32_e32 v68, -3, v2
	s_nop 0
	v_cndmask_b32_e32 v168, v189, v168, vcc
	v_cmp_lt_i32_e32 vcc, -1, v68
	s_nop 1
	v_cndmask_b32_e32 v161, v189, v161, vcc
	v_cmp_lt_i32_e32 vcc, 31, v68
	v_add_u32_e32 v68, -8, v2
	s_nop 0
	v_cndmask_b32_e32 v169, v189, v169, vcc
	v_cmp_lt_i32_e32 vcc, -1, v68
	s_nop 1
	v_cndmask_b32_e32 v154, v189, v154, vcc
	v_cmp_lt_i32_e32 vcc, 31, v68
	v_add_u32_e32 v68, -9, v2
	s_nop 0
	v_cndmask_b32_e32 v164, v189, v164, vcc
	v_cmp_lt_i32_e32 vcc, -1, v68
	s_nop 1
	v_cndmask_b32_e32 v155, v189, v155, vcc
	v_cmp_lt_i32_e32 vcc, 31, v68
	v_add_u32_e32 v68, -10, v2
	s_nop 0
	v_cndmask_b32_e32 v165, v189, v165, vcc
	v_cmp_lt_i32_e32 vcc, -1, v68
	s_nop 1
	v_cndmask_b32_e32 v150, v189, v150, vcc
	v_cmp_lt_i32_e32 vcc, 31, v68
	v_add_u32_e32 v68, -11, v2
	s_nop 0
	v_cndmask_b32_e32 v162, v189, v162, vcc
	v_cmp_lt_i32_e32 vcc, -1, v68
	s_nop 1
	v_cndmask_b32_e32 v151, v189, v151, vcc
	v_cmp_lt_i32_e32 vcc, 31, v68
	v_add_u32_e32 v68, -16, v2
	s_nop 0
	v_cndmask_b32_e32 v163, v189, v163, vcc
	v_cmp_lt_i32_e32 vcc, -1, v68
	s_nop 1
	v_cndmask_b32_e32 v144, v189, v144, vcc
	v_cmp_lt_i32_e32 vcc, 31, v68
	v_subrev_u32_e32 v68, 17, v2
	s_nop 0
	v_cndmask_b32_e32 v156, v189, v156, vcc
	v_cmp_lt_i32_e32 vcc, -1, v68
	s_nop 1
	v_cndmask_b32_e32 v145, v189, v145, vcc
	v_cmp_lt_i32_e32 vcc, 31, v68
	v_subrev_u32_e32 v68, 18, v2
	s_nop 0
	v_cndmask_b32_e32 v157, v189, v157, vcc
	v_cmp_lt_i32_e32 vcc, -1, v68
	s_nop 1
	v_cndmask_b32_e32 v146, v189, v146, vcc
	v_cmp_lt_i32_e32 vcc, 31, v68
	v_subrev_u32_e32 v68, 19, v2
	s_nop 0
	v_cndmask_b32_e32 v158, v189, v158, vcc
	v_cmp_lt_i32_e32 vcc, -1, v68
	s_nop 1
	v_cndmask_b32_e32 v147, v189, v147, vcc
	v_cmp_lt_i32_e32 vcc, 31, v68
	v_subrev_u32_e32 v68, 24, v2
	s_nop 0
	v_cndmask_b32_e32 v159, v189, v159, vcc
	v_cmp_lt_i32_e32 vcc, -1, v68
	s_nop 1
	v_cndmask_b32_e32 v142, v189, v142, vcc
	v_cmp_lt_i32_e32 vcc, 31, v68
	v_subrev_u32_e32 v68, 25, v2
	s_nop 0
	v_cndmask_b32_e32 v152, v189, v152, vcc
	v_cmp_lt_i32_e32 vcc, -1, v68
	s_nop 1
	v_cndmask_b32_e32 v143, v189, v143, vcc
	v_cmp_lt_i32_e32 vcc, 31, v68
	v_subrev_u32_e32 v68, 26, v2
	v_subrev_u32_e32 v2, 27, v2
	v_cndmask_b32_e32 v153, v189, v153, vcc
	v_cmp_lt_i32_e32 vcc, -1, v68
	s_nop 1
	v_cndmask_b32_e32 v140, v189, v140, vcc
	v_cmp_lt_i32_e32 vcc, 31, v68
	s_nop 1
	v_cndmask_b32_e32 v148, v189, v148, vcc
	v_cmp_lt_i32_e32 vcc, -1, v2
	s_nop 1
	v_cndmask_b32_e32 v141, v189, v141, vcc
	v_cmp_lt_i32_e32 vcc, 31, v2
	s_nop 1
	v_cndmask_b32_e32 v149, v189, v149, vcc

.LBB0_1460:
	ds_read_b64_tr_b16 v[76:77], v174 offset:0
	ds_read_b64_tr_b16 v[78:79], v174 offset:0x800
	ds_read_b64_tr_b16 v[80:81], v174 offset:0x1000
	v_add_f32_e32 v140, v83, v140
	ds_read_b64_tr_b16 v[82:83], v174 offset:0x1800
	ds_read_b64_tr_b16 v[92:93], v174 offset:0x2000
	ds_read_b64_tr_b16 v[94:95], v174 offset:0x2800
	ds_read_b64_tr_b16 v[96:97], v174 offset:0x3000
	ds_read_b64_tr_b16 v[98:99], v174 offset:0x3800
	v_fmac_f32_e32 v140, v191, v2
	s_waitcnt lgkmcnt(6)
	v_mfma_f32_32x32x16_bf16 v[52:67], v[76:79], v[84:87], v[52:67]
	ds_read_b64_tr_b16 v[76:77], v174 offset:0x200
	ds_read_b64_tr_b16 v[78:79], v174 offset:0xa00
	s_waitcnt lgkmcnt(6)
	v_mfma_f32_32x32x16_bf16 v[52:67], v[80:83], v[88:91], v[52:67]
	ds_read_b64_tr_b16 v[80:81], v174 offset:0x1200
	ds_read_b64_tr_b16 v[82:83], v174 offset:0x1a00
	s_waitcnt lgkmcnt(6)
	v_mfma_f32_32x32x16_bf16 v[52:67], v[92:95], v[68:71], v[52:67]
	ds_read_b64_tr_b16 v[92:93], v174 offset:0x2200
	ds_read_b64_tr_b16 v[94:95], v174 offset:0x2a00
	s_waitcnt lgkmcnt(6)
	v_mfma_f32_32x32x16_bf16 v[52:67], v[96:99], v[72:75], v[52:67]
	ds_read_b64_tr_b16 v[96:97], v174 offset:0x3200
	ds_read_b64_tr_b16 v[98:99], v174 offset:0x3a00
	s_waitcnt lgkmcnt(6)
	v_mfma_f32_32x32x16_bf16 v[36:51], v[76:79], v[84:87], v[36:51]
	ds_read_b64_tr_b16 v[76:77], v174 offset:0x400
	ds_read_b64_tr_b16 v[78:79], v174 offset:0xc00
	s_waitcnt lgkmcnt(6)
	v_mfma_f32_32x32x16_bf16 v[36:51], v[80:83], v[88:91], v[36:51]
	ds_read_b64_tr_b16 v[80:81], v174 offset:0x1400
	ds_read_b64_tr_b16 v[82:83], v174 offset:0x1c00
	s_waitcnt lgkmcnt(6)
	v_mfma_f32_32x32x16_bf16 v[36:51], v[92:95], v[68:71], v[36:51]
	ds_read_b64_tr_b16 v[92:93], v174 offset:0x2400
	ds_read_b64_tr_b16 v[94:95], v174 offset:0x2c00
	s_waitcnt lgkmcnt(6)
	v_mfma_f32_32x32x16_bf16 v[36:51], v[96:99], v[72:75], v[36:51]
	ds_read_b64_tr_b16 v[96:97], v174 offset:0x3400
	ds_read_b64_tr_b16 v[98:99], v174 offset:0x3c00
	s_waitcnt lgkmcnt(6)
	v_mfma_f32_32x32x16_bf16 v[20:35], v[76:79], v[84:87], v[20:35]
	ds_read_b64_tr_b16 v[76:77], v174 offset:0x600
	ds_read_b64_tr_b16 v[78:79], v174 offset:0xe00
	s_waitcnt lgkmcnt(6)
	v_mfma_f32_32x32x16_bf16 v[20:35], v[80:83], v[88:91], v[20:35]
	ds_read_b64_tr_b16 v[80:81], v174 offset:0x1600
	ds_read_b64_tr_b16 v[82:83], v174 offset:0x1e00
	s_waitcnt lgkmcnt(6)
	v_mfma_f32_32x32x16_bf16 v[20:35], v[92:95], v[68:71], v[20:35]
	ds_read_b64_tr_b16 v[92:93], v174 offset:0x2600
	ds_read_b64_tr_b16 v[94:95], v174 offset:0x2e00
	s_waitcnt lgkmcnt(6)
	v_mfma_f32_32x32x16_bf16 v[20:35], v[96:99], v[72:75], v[20:35]
	ds_read_b64_tr_b16 v[96:97], v174 offset:0x3600
	ds_read_b64_tr_b16 v[98:99], v174 offset:0x3e00
	s_waitcnt lgkmcnt(6)
	v_mfma_f32_32x32x16_bf16 v[4:19], v[76:79], v[84:87], v[4:19]
	s_waitcnt lgkmcnt(4)
	v_mfma_f32_32x32x16_bf16 v[4:19], v[80:83], v[88:91], v[4:19]
	s_waitcnt lgkmcnt(2)
	v_mfma_f32_32x32x16_bf16 v[4:19], v[92:95], v[68:71], v[4:19]
	s_waitcnt lgkmcnt(0)
	v_mfma_f32_32x32x16_bf16 v[4:19], v[96:99], v[72:75], v[4:19]
	s_setprio 0
	v_mov_b32_e32 v191, v140
	s_and_b64 vcc, exec, s[4:5]
	s_cbranch_vccz .LBB0_1438
	s_branch .LBB0_1439

.LBB0_1467:
	ds_read_b128 v[208:211], v172 offset:49152
	ds_read_b128 v[212:215], v172 offset:57344
	ds_read_b128 v[216:219], v206 offset:49152
	ds_read_b128 v[220:223], v206 offset:57344
	ds_read_b128 v[224:227], v207 offset:49152
	ds_read_b128 v[228:231], v207 offset:57344
	ds_read_b128 v[232:235], v237 offset:49152
	ds_read_b128 v[238:241], v237 offset:57344
	s_waitcnt lgkmcnt(7)
	v_mfma_f32_32x32x16_bf16 v[84:99], v[208:211], v[100:103], 0
	ds_read_b128 v[208:211], v244 offset:49152
	s_waitcnt lgkmcnt(7)
	v_mfma_f32_32x32x16_bf16 v[68:83], v[212:215], v[100:103], 0
	ds_read_b128 v[212:215], v244 offset:57344
	s_waitcnt lgkmcnt(7)
	v_mfma_f32_32x32x16_bf16 v[84:99], v[216:219], v[104:107], v[84:99]
	ds_read_b128 v[216:219], v245 offset:49152
	s_waitcnt lgkmcnt(7)
	v_mfma_f32_32x32x16_bf16 v[68:83], v[220:223], v[104:107], v[68:83]
	ds_read_b128 v[220:223], v245 offset:57344
	s_waitcnt lgkmcnt(7)
	v_mfma_f32_32x32x16_bf16 v[84:99], v[224:227], v[108:111], v[84:99]
	ds_read_b128 v[224:227], v246 offset:49152
	s_waitcnt lgkmcnt(7)
	v_mfma_f32_32x32x16_bf16 v[68:83], v[228:231], v[108:111], v[68:83]
	ds_read_b128 v[228:231], v246 offset:57344
	s_waitcnt lgkmcnt(7)
	v_mfma_f32_32x32x16_bf16 v[84:99], v[232:235], v[112:115], v[84:99]
	ds_read_b128 v[232:235], v247 offset:49152
	s_waitcnt lgkmcnt(7)
	v_mfma_f32_32x32x16_bf16 v[68:83], v[238:241], v[112:115], v[68:83]
	ds_read_b128 v[238:241], v247 offset:57344
	s_waitcnt lgkmcnt(7)
	v_mfma_f32_32x32x16_bf16 v[84:99], v[208:211], v[116:119], v[84:99]
	s_waitcnt lgkmcnt(6)
	v_mfma_f32_32x32x16_bf16 v[68:83], v[212:215], v[116:119], v[68:83]
	s_waitcnt lgkmcnt(5)
	v_mfma_f32_32x32x16_bf16 v[84:99], v[216:219], v[120:123], v[84:99]
	s_waitcnt lgkmcnt(4)
	v_mfma_f32_32x32x16_bf16 v[68:83], v[220:223], v[120:123], v[68:83]
	s_waitcnt lgkmcnt(3)
	v_mfma_f32_32x32x16_bf16 v[84:99], v[224:227], v[124:127], v[84:99]
	s_waitcnt lgkmcnt(2)
	v_mfma_f32_32x32x16_bf16 v[68:83], v[228:231], v[124:127], v[68:83]
	s_waitcnt lgkmcnt(1)
	v_mfma_f32_32x32x16_bf16 v[84:99], v[232:235], v[128:131], v[84:99]
	s_waitcnt lgkmcnt(0)
	v_mfma_f32_32x32x16_bf16 v[68:83], v[238:241], v[128:131], v[68:83]
	ds_read_b128 v[156:159], v177
	ds_read_b128 v[194:197], v177 offset:128
	ds_read_b128 v[140:143], v177 offset:32
	ds_read_b128 v[168:171], v177 offset:160
	ds_read_b128 v[144:147], v177 offset:64
	ds_read_b128 v[198:201], v177 offset:192
	ds_read_b128 v[162:165], v177 offset:96
	ds_read_b128 v[202:205], v177 offset:224
	s_waitcnt lgkmcnt(3)
	v_pk_add_f32 v[144:145], v[92:93], v[144:145]
	v_pk_add_f32 v[150:151], v[90:91], v[142:143]
	v_pk_add_f32 v[154:155], v[88:89], v[140:141]
	v_pk_add_f32 v[160:161], v[86:87], v[158:159]
	v_pk_add_f32 v[146:147], v[94:95], v[146:147]
	s_waitcnt lgkmcnt(1)
	v_pk_add_f32 v[142:143], v[96:97], v[162:163]
	v_pk_add_f32 v[140:141], v[98:99], v[164:165]
	v_pk_add_f32 v[166:167], v[84:85], v[156:157]
	v_pk_add_f32 v[156:157], v[76:77], v[198:199]
	v_pk_add_f32 v[162:163], v[74:75], v[170:171]
	v_pk_add_f32 v[164:165], v[72:73], v[168:169]
	v_pk_add_f32 v[168:169], v[70:71], v[196:197]
	v_pk_add_f32 v[158:159], v[78:79], v[200:201]
	s_waitcnt lgkmcnt(0)
	v_pk_add_f32 v[152:153], v[80:81], v[202:203]
	v_pk_add_f32 v[148:149], v[82:83], v[204:205]
	v_pk_add_f32 v[170:171], v[68:69], v[194:195]
	s_add_i32 s8, s18, 64
	s_cmp_le_i32 s8, s40
	s_cbranch_scc1 .LBB0_1469
	v_add_u32_e32 v2, s71, v190
	v_subrev_u32_e32 v68, 64, v2
	v_cmp_lt_i32_e32 vcc, -1, v68
	s_nop 1
	v_cndmask_b32_e32 v166, v189, v166, vcc
	v_cmp_lt_i32_e32 vcc, 31, v68
	v_add_u32_e32 v68, 0xffffffbf, v2
	s_nop 0
	v_cndmask_b32_e32 v170, v189, v170, vcc
	v_cmp_lt_i32_e32 vcc, -1, v68
	s_nop 1
	v_cndmask_b32_e32 v167, v189, v167, vcc
	v_cmp_lt_i32_e32 vcc, 31, v68
	v_add_u32_e32 v68, 0xffffffbe, v2
	s_nop 0
	v_cndmask_b32_e32 v171, v189, v171, vcc
	v_cmp_lt_i32_e32 vcc, -1, v68
	s_nop 1
	v_cndmask_b32_e32 v160, v189, v160, vcc
	v_cmp_lt_i32_e32 vcc, 31, v68
	v_add_u32_e32 v68, 0xffffffbd, v2
	s_nop 0
	v_cndmask_b32_e32 v168, v189, v168, vcc
	v_cmp_lt_i32_e32 vcc, -1, v68
	s_nop 1
	v_cndmask_b32_e32 v161, v189, v161, vcc
	v_cmp_lt_i32_e32 vcc, 31, v68
	v_add_u32_e32 v68, 0xffffffb8, v2
	s_nop 0
	v_cndmask_b32_e32 v169, v189, v169, vcc
	v_cmp_lt_i32_e32 vcc, -1, v68
	s_nop 1
	v_cndmask_b32_e32 v154, v189, v154, vcc
	v_cmp_lt_i32_e32 vcc, 31, v68
	v_add_u32_e32 v68, 0xffffffb7, v2
	s_nop 0
	v_cndmask_b32_e32 v164, v189, v164, vcc
	v_cmp_lt_i32_e32 vcc, -1, v68
	s_nop 1
	v_cndmask_b32_e32 v155, v189, v155, vcc
	v_cmp_lt_i32_e32 vcc, 31, v68
	v_add_u32_e32 v68, 0xffffffb6, v2
	s_nop 0
	v_cndmask_b32_e32 v165, v189, v165, vcc
	v_cmp_lt_i32_e32 vcc, -1, v68
	s_nop 1
	v_cndmask_b32_e32 v150, v189, v150, vcc
	v_cmp_lt_i32_e32 vcc, 31, v68
	v_add_u32_e32 v68, 0xffffffb5, v2
	s_nop 0
	v_cndmask_b32_e32 v162, v189, v162, vcc
	v_cmp_lt_i32_e32 vcc, -1, v68
	s_nop 1
	v_cndmask_b32_e32 v151, v189, v151, vcc
	v_cmp_lt_i32_e32 vcc, 31, v68
	v_add_u32_e32 v68, 0xffffffb0, v2
	s_nop 0
	v_cndmask_b32_e32 v163, v189, v163, vcc
	v_cmp_lt_i32_e32 vcc, -1, v68
	s_nop 1
	v_cndmask_b32_e32 v144, v189, v144, vcc
	v_cmp_lt_i32_e32 vcc, 31, v68
	v_add_u32_e32 v68, 0xffffffaf, v2
	s_nop 0
	v_cndmask_b32_e32 v156, v189, v156, vcc
	v_cmp_lt_i32_e32 vcc, -1, v68
	s_nop 1
	v_cndmask_b32_e32 v145, v189, v145, vcc
	v_cmp_lt_i32_e32 vcc, 31, v68
	v_add_u32_e32 v68, 0xffffffae, v2
	s_nop 0
	v_cndmask_b32_e32 v157, v189, v157, vcc
	v_cmp_lt_i32_e32 vcc, -1, v68
	s_nop 1
	v_cndmask_b32_e32 v146, v189, v146, vcc
	v_cmp_lt_i32_e32 vcc, 31, v68
	v_add_u32_e32 v68, 0xffffffad, v2
	s_nop 0
	v_cndmask_b32_e32 v158, v189, v158, vcc
	v_cmp_lt_i32_e32 vcc, -1, v68
	s_nop 1
	v_cndmask_b32_e32 v147, v189, v147, vcc
	v_cmp_lt_i32_e32 vcc, 31, v68
	v_add_u32_e32 v68, 0xffffffa8, v2
	s_nop 0
	v_cndmask_b32_e32 v159, v189, v159, vcc
	v_cmp_lt_i32_e32 vcc, -1, v68
	s_nop 1
	v_cndmask_b32_e32 v142, v189, v142, vcc
	v_cmp_lt_i32_e32 vcc, 31, v68
	v_add_u32_e32 v68, 0xffffffa7, v2
	s_nop 0
	v_cndmask_b32_e32 v152, v189, v152, vcc
	v_cmp_lt_i32_e32 vcc, -1, v68
	s_nop 1
	v_cndmask_b32_e32 v143, v189, v143, vcc
	v_cmp_lt_i32_e32 vcc, 31, v68
	v_add_u32_e32 v68, 0xffffffa6, v2
	v_add_u32_e32 v2, 0xffffffa5, v2
	v_cndmask_b32_e32 v153, v189, v153, vcc
	v_cmp_lt_i32_e32 vcc, -1, v68
	s_nop 1
	v_cndmask_b32_e32 v140, v189, v140, vcc
	v_cmp_lt_i32_e32 vcc, 31, v68
	s_nop 1
	v_cndmask_b32_e32 v148, v189, v148, vcc
	v_cmp_lt_i32_e32 vcc, -1, v2
	s_nop 1
	v_cndmask_b32_e32 v141, v189, v141, vcc
	v_cmp_lt_i32_e32 vcc, 31, v2
	s_nop 1
	v_cndmask_b32_e32 v149, v189, v149, vcc

.LBB0_1475:
	ds_read_b64_tr_b16 v[76:77], v174 offset:0x4000
	ds_read_b64_tr_b16 v[78:79], v174 offset:0x4800
	ds_read_b64_tr_b16 v[80:81], v174 offset:0x5000
	v_add_f32_e32 v140, v83, v140
	ds_read_b64_tr_b16 v[82:83], v174 offset:0x5800
	ds_read_b64_tr_b16 v[92:93], v174 offset:0x6000
	ds_read_b64_tr_b16 v[94:95], v174 offset:0x6800
	ds_read_b64_tr_b16 v[96:97], v174 offset:0x7000
	ds_read_b64_tr_b16 v[98:99], v174 offset:0x7800
	v_fmac_f32_e32 v140, v191, v2
	s_waitcnt lgkmcnt(6)
	v_mfma_f32_32x32x16_bf16 v[52:67], v[76:79], v[84:87], v[52:67]
	ds_read_b64_tr_b16 v[76:77], v174 offset:0x4200
	ds_read_b64_tr_b16 v[78:79], v174 offset:0x4a00
	s_waitcnt lgkmcnt(6)
	v_mfma_f32_32x32x16_bf16 v[52:67], v[80:83], v[88:91], v[52:67]
	ds_read_b64_tr_b16 v[80:81], v174 offset:0x5200
	ds_read_b64_tr_b16 v[82:83], v174 offset:0x5a00
	s_waitcnt lgkmcnt(6)
	v_mfma_f32_32x32x16_bf16 v[52:67], v[92:95], v[68:71], v[52:67]
	ds_read_b64_tr_b16 v[92:93], v174 offset:0x6200
	ds_read_b64_tr_b16 v[94:95], v174 offset:0x6a00
	s_waitcnt lgkmcnt(6)
	v_mfma_f32_32x32x16_bf16 v[52:67], v[96:99], v[72:75], v[52:67]
	ds_read_b64_tr_b16 v[96:97], v174 offset:0x7200
	ds_read_b64_tr_b16 v[98:99], v174 offset:0x7a00
	s_waitcnt lgkmcnt(6)
	v_mfma_f32_32x32x16_bf16 v[36:51], v[76:79], v[84:87], v[36:51]
	ds_read_b64_tr_b16 v[76:77], v174 offset:0x4400
	ds_read_b64_tr_b16 v[78:79], v174 offset:0x4c00
	s_waitcnt lgkmcnt(6)
	v_mfma_f32_32x32x16_bf16 v[36:51], v[80:83], v[88:91], v[36:51]
	ds_read_b64_tr_b16 v[80:81], v174 offset:0x5400
	ds_read_b64_tr_b16 v[82:83], v174 offset:0x5c00
	s_waitcnt lgkmcnt(6)
	v_mfma_f32_32x32x16_bf16 v[36:51], v[92:95], v[68:71], v[36:51]
	ds_read_b64_tr_b16 v[92:93], v174 offset:0x6400
	ds_read_b64_tr_b16 v[94:95], v174 offset:0x6c00
	s_waitcnt lgkmcnt(6)
	v_mfma_f32_32x32x16_bf16 v[36:51], v[96:99], v[72:75], v[36:51]
	ds_read_b64_tr_b16 v[96:97], v174 offset:0x7400
	ds_read_b64_tr_b16 v[98:99], v174 offset:0x7c00
	s_waitcnt lgkmcnt(6)
	v_mfma_f32_32x32x16_bf16 v[20:35], v[76:79], v[84:87], v[20:35]
	ds_read_b64_tr_b16 v[76:77], v174 offset:0x4600
	ds_read_b64_tr_b16 v[78:79], v174 offset:0x4e00
	s_waitcnt lgkmcnt(6)
	v_mfma_f32_32x32x16_bf16 v[20:35], v[80:83], v[88:91], v[20:35]
	ds_read_b64_tr_b16 v[80:81], v174 offset:0x5600
	ds_read_b64_tr_b16 v[82:83], v174 offset:0x5e00
	s_waitcnt lgkmcnt(6)
	v_mfma_f32_32x32x16_bf16 v[20:35], v[92:95], v[68:71], v[20:35]
	ds_read_b64_tr_b16 v[92:93], v174 offset:0x6600
	ds_read_b64_tr_b16 v[94:95], v174 offset:0x6e00
	s_waitcnt lgkmcnt(6)
	v_mfma_f32_32x32x16_bf16 v[20:35], v[96:99], v[72:75], v[20:35]
	ds_read_b64_tr_b16 v[96:97], v174 offset:0x7600
	ds_read_b64_tr_b16 v[98:99], v174 offset:0x7e00
	s_waitcnt lgkmcnt(6)
	v_mfma_f32_32x32x16_bf16 v[4:19], v[76:79], v[84:87], v[4:19]
	s_waitcnt lgkmcnt(4)
	v_mfma_f32_32x32x16_bf16 v[4:19], v[80:83], v[88:91], v[4:19]
	s_waitcnt lgkmcnt(2)
	v_mfma_f32_32x32x16_bf16 v[4:19], v[92:95], v[68:71], v[4:19]
	s_waitcnt lgkmcnt(0)
	v_mfma_f32_32x32x16_bf16 v[4:19], v[96:99], v[72:75], v[4:19]
	s_setprio 0
	v_mov_b32_e32 v191, v140
	s_branch .LBB0_1427

; #define LAS __attribute__((address_space(3)))
; __global__ void __launch_bounds__(NTHREADS, 2) fwd(Args a) {
;     extern __shared__ __attribute__((aligned(16))) unsigned char lds_raw[];
;     LAS unsigned char* lds = (LAS unsigned char*)lds_raw;
;     (void)a;
	.amdhsa_kernel _Z3fwd4Args
		.amdhsa_group_segment_fixed_size 0
		.amdhsa_private_segment_fixed_size 0
		.amdhsa_kernarg_size 504
		.amdhsa_user_sgpr_count 2
		.amdhsa_user_sgpr_dispatch_ptr 0
		.amdhsa_user_sgpr_queue_ptr 0
		.amdhsa_user_sgpr_kernarg_segment_ptr 1
		.amdhsa_user_sgpr_dispatch_id 0
		.amdhsa_user_sgpr_kernarg_preload_length 0
		.amdhsa_user_sgpr_kernarg_preload_offset 0
		.amdhsa_user_sgpr_private_segment_size 0
		.amdhsa_uses_dynamic_stack 0
		.amdhsa_enable_private_segment 0
		.amdhsa_system_sgpr_workgroup_id_x 1
		.amdhsa_system_sgpr_workgroup_id_y 0
		.amdhsa_system_sgpr_workgroup_id_z 0
		.amdhsa_system_sgpr_workgroup_info 0
		.amdhsa_system_vgpr_workitem_id 0
		.amdhsa_next_free_vgpr 253
		.amdhsa_next_free_sgpr 102
		.amdhsa_accum_offset 256
		.amdhsa_reserve_vcc 1
		.amdhsa_float_round_mode_32 0
		.amdhsa_float_round_mode_16_64 0
		.amdhsa_float_denorm_mode_32 3
		.amdhsa_float_denorm_mode_16_64 3
		.amdhsa_dx10_clamp 1
		.amdhsa_ieee_mode 1
		.amdhsa_fp16_overflow 0
		.amdhsa_tg_split 0
		.amdhsa_exception_fp_ieee_invalid_op 0
		.amdhsa_exception_fp_denorm_src 0
		.amdhsa_exception_fp_ieee_div_zero 0
		.amdhsa_exception_fp_ieee_overflow 0
		.amdhsa_exception_fp_ieee_underflow 0
		.amdhsa_exception_fp_ieee_inexact 0
		.amdhsa_exception_int_div_zero 0
	.end_amdhsa_kernel

; #define LAS __attribute__((address_space(3)))
; __global__ void __launch_bounds__(NTHREADS, 2) fwd(Args a) {
;     extern __shared__ __attribute__((aligned(16))) unsigned char lds_raw[];
;     LAS unsigned char* lds = (LAS unsigned char*)lds_raw;
;     (void)a;
amdhsa.kernels:
  - .agpr_count:     0
    .args:
      - .offset:         0
        .size:           248
        .value_kind:     by_value
      - .offset:         248
        .size:           4
        .value_kind:     hidden_block_count_x
      - .offset:         252
        .size:           4
        .value_kind:     hidden_block_count_y
      - .offset:         256
        .size:           4
        .value_kind:     hidden_block_count_z
      - .offset:         260
        .size:           2
        .value_kind:     hidden_group_size_x
      - .offset:         262
        .size:           2
        .value_kind:     hidden_group_size_y
      - .offset:         264
        .size:           2
        .value_kind:     hidden_group_size_z
      - .offset:         266
        .size:           2
        .value_kind:     hidden_remainder_x
      - .offset:         268
        .size:           2
        .value_kind:     hidden_remainder_y
      - .offset:         270
        .size:           2
        .value_kind:     hidden_remainder_z
      - .offset:         288
        .size:           8
        .value_kind:     hidden_global_offset_x
      - .offset:         296
        .size:           8
        .value_kind:     hidden_global_offset_y
      - .offset:         304
        .size:           8
        .value_kind:     hidden_global_offset_z
      - .offset:         312
        .size:           2
        .value_kind:     hidden_grid_dims
      - .offset:         368
        .size:           4
        .value_kind:     hidden_dynamic_lds_size
    .group_segment_fixed_size: 0
    .kernarg_segment_align: 8
    .kernarg_segment_size: 504
    .language:       OpenCL C
    .language_version:
      - 2
      - 0
    .max_flat_workgroup_size: 512
    .name:           _Z3fwd4Args
    .private_segment_fixed_size: 0
    .sgpr_count:     108
    .sgpr_spill_count: 56
    .symbol:         _Z3fwd4Args.kd
    .uniform_work_group_size: 1
    .uses_dynamic_stack: false
    .vgpr_count:     253
    .vgpr_spill_count: 0
    .wavefront_size: 64
